# diff-attention: softmax head takes the rare running-max path only when the tile max exceeds the reference by 8; per-half row sums combined once in the unit epilogue
# baseline (speedup 1.0000x reference)
.LBB0_563:
	v_mov_b32_e32 v230, 0xff800000
	v_mov_b32_e32 v228, v251
	v_mov_b32_e32 v229, v208
	s_nop 1
	v_permlane32_swap_b32_e32 v251, v228
	v_permlane32_swap_b32_e32 v208, v229
	v_add_f32_e32 v251, v251, v228
	v_add_f32_e32 v208, v208, v229
	s_or_b32 s14, s39, s35
	s_mul_hi_i32 s18, s14, 0x1a00
	s_mul_i32 s16, s14, 0x1a00
	v_div_scale_f32 v129, s[14:15], v251, v251, 1.0
	v_rcp_f32_e32 v130, v129
	s_add_u32 s14, s36, s16
	v_div_scale_f32 v147, s[16:17], v208, v208, v232
	v_fma_f32 v131, -v129, v130, 1.0
	v_fmac_f32_e32 v130, v131, v130
	v_div_scale_f32 v131, vcc, 1.0, v251, 1.0
	v_rcp_f32_e32 v148, v147
	v_mul_f32_e32 v132, v131, v130
	v_fma_f32 v133, -v129, v132, v131
	v_fmac_f32_e32 v132, v133, v130
	v_fma_f32 v129, -v129, v132, v131
	v_fma_f32 v149, -v147, v148, 1.0
	v_div_fmas_f32 v129, v129, v130, v132
	v_fmac_f32_e32 v148, v149, v148
	v_div_scale_f32 v149, vcc, v232, v208, v232
	v_mul_f32_e32 v150, v149, v148
	v_fma_f32 v151, -v147, v150, v149
	v_fmac_f32_e32 v150, v151, v148
	v_fma_f32 v147, -v147, v150, v149
	v_div_fixup_f32 v129, v129, v251, 1.0
	v_ashrrev_i32_e32 v128, 5, v235
	v_lshl_add_u32 v146, v235, 2, s40
	v_div_fmas_f32 v147, v147, v148, v150
	ds_write_b32 v146, v129
	v_lshl_add_u32 v129, v128, 4, s40
	v_div_fixup_f32 v147, v147, v208, v232
	ds_read_b128 v[130:133], v129
	ds_read_b128 v[134:137], v129 offset:32
	ds_read_b128 v[138:141], v129 offset:64
	ds_read_b128 v[142:145], v129 offset:96
	ds_write_b32 v146, v147
	ds_read_b128 v[146:149], v129
	ds_read_b128 v[150:153], v129 offset:32
	ds_read_b128 v[154:157], v129 offset:64
	ds_read_b128 v[158:161], v129 offset:96
	s_addc_u32 s15, s37, s18
	s_waitcnt lgkmcnt(3)
	v_mul_f32_e32 v112, v112, v146
	v_fma_f32 v129, v64, v130, -v112
	v_mul_f32_e32 v64, v113, v147
	v_fma_f32 v113, v65, v131, -v64
	v_mul_f32_e32 v64, v114, v148
	v_fma_f32 v114, v66, v132, -v64
	v_mul_f32_e32 v64, v115, v149
	v_fma_f32 v115, v67, v133, -v64
	s_waitcnt lgkmcnt(2)
	v_mul_f32_e32 v64, v116, v150
	v_fma_f32 v116, v68, v134, -v64
	v_mul_f32_e32 v64, v117, v151
	v_fma_f32 v117, v69, v135, -v64
	v_mul_f32_e32 v64, v118, v152
	v_fma_f32 v118, v70, v136, -v64
	v_mul_f32_e32 v64, v119, v153
	v_fma_f32 v112, v71, v137, -v64
	s_waitcnt lgkmcnt(1)
	v_mul_f32_e32 v64, v120, v154
	v_fma_f32 v71, v72, v138, -v64
	v_mul_f32_e32 v72, v96, v146
	v_mul_f32_e32 v64, v121, v155
	v_fma_f32 v72, v32, v130, -v72
	v_mul_f32_e32 v32, v97, v147
	v_fma_f32 v70, v73, v139, -v64
	v_mul_f32_e32 v64, v122, v156
	v_fma_f32 v73, v33, v131, -v32
	v_mul_f32_e32 v32, v98, v148
	v_fma_f32 v69, v74, v140, -v64
	v_mul_f32_e32 v64, v123, v157
	v_fma_f32 v74, v34, v132, -v32
	v_mul_f32_e32 v32, v99, v149
	v_fma_f32 v68, v75, v141, -v64
	s_waitcnt lgkmcnt(0)
	v_mul_f32_e32 v64, v124, v158
	v_fma_f32 v75, v35, v133, -v32
	v_mul_f32_e32 v32, v100, v150
	v_fma_f32 v67, v76, v142, -v64
	v_mul_f32_e32 v64, v125, v159
	v_fma_f32 v76, v36, v134, -v32
	v_mul_f32_e32 v32, v101, v151
	v_fma_f32 v66, v77, v143, -v64
	v_mul_f32_e32 v64, v126, v160
	v_fma_f32 v77, v37, v135, -v32
	v_mul_f32_e32 v32, v102, v152
	v_fma_f32 v65, v78, v144, -v64
	v_mul_f32_e32 v64, v127, v161
	v_fma_f32 v78, v38, v136, -v32
	v_mul_f32_e32 v32, v103, v153
	v_fma_f32 v64, v79, v145, -v64
	v_fma_f32 v79, v39, v137, -v32
	v_mul_f32_e32 v32, v104, v154
	v_fma_f32 v39, v40, v138, -v32
	v_mul_f32_e32 v32, v105, v155
	v_fma_f32 v38, v41, v139, -v32
	v_mul_f32_e32 v32, v106, v156
	v_fma_f32 v37, v42, v140, -v32
	v_mul_f32_e32 v32, v107, v157
	v_fma_f32 v36, v43, v141, -v32
	v_mul_f32_e32 v32, v108, v158
	v_mul_f32_e32 v40, v80, v146
	v_fma_f32 v35, v44, v142, -v32
	v_mul_f32_e32 v32, v109, v159
	v_fma_f32 v42, v16, v130, -v40
	v_mul_f32_e32 v16, v81, v147
	v_fma_f32 v34, v45, v143, -v32
	v_mul_f32_e32 v32, v110, v160
	v_fma_f32 v43, v17, v131, -v16
	v_mul_f32_e32 v16, v82, v148
	v_fma_f32 v33, v46, v144, -v32
	v_mul_f32_e32 v32, v111, v161
	v_fma_f32 v44, v18, v132, -v16
	v_mul_f32_e32 v16, v83, v149
	v_fma_f32 v32, v47, v145, -v32
	v_fma_f32 v47, v19, v133, -v16
	v_mul_f32_e32 v16, v84, v150
	v_fma_f32 v80, v20, v134, -v16
	v_mul_f32_e32 v16, v85, v151
	v_fma_f32 v81, v21, v135, -v16
	v_mul_f32_e32 v16, v86, v152
	v_fma_f32 v82, v22, v136, -v16
	v_mul_f32_e32 v16, v87, v153
	v_and_b32_e32 v17, 31, v235
	v_fma_f32 v83, v23, v137, -v16
	v_mul_f32_e32 v16, v88, v154
	v_lshlrev_b32_e32 v23, 2, v17
	v_fma_f32 v41, v24, v138, -v16
	global_load_dword v24, v23, s[4:5]
	v_mul_f32_e32 v16, v89, v155
	v_fma_f32 v40, v25, v139, -v16
	v_mul_f32_e32 v16, v90, v156
	v_fma_f32 v22, v26, v140, -v16
	v_mul_f32_e32 v16, v91, v157
	v_fma_f32 v21, v27, v141, -v16
	v_mul_f32_e32 v16, v92, v158
	v_fma_f32 v20, v28, v142, -v16
	global_load_dword v26, v23, s[4:5] offset:128
	global_load_dword v27, v23, s[4:5] offset:256
	global_load_dword v28, v23, s[4:5] offset:384
	v_mul_f32_e32 v25, v48, v146
	v_mul_f32_e32 v18, v94, v160
	v_fma_f32 v25, v0, v130, -v25
	v_mul_f32_e32 v0, v49, v147
	v_fma_f32 v19, v30, v144, -v18
	v_fma_f32 v30, v1, v131, -v0
	v_mul_f32_e32 v0, v50, v148
	v_fma_f32 v45, v2, v132, -v0
	v_mul_f32_e32 v0, v51, v149
	v_fma_f32 v48, v3, v133, -v0
	v_mul_f32_e32 v0, v52, v150
	v_fma_f32 v49, v4, v134, -v0
	v_mul_f32_e32 v0, v53, v151
	v_fma_f32 v50, v5, v135, -v0
	v_mul_f32_e32 v0, v54, v152
	v_fma_f32 v51, v6, v136, -v0
	v_mul_f32_e32 v0, v55, v153
	v_fma_f32 v52, v7, v137, -v0
	v_mul_f32_e32 v0, v56, v154
	v_and_b32_e32 v5, 64, v225
	v_fma_f32 v53, v8, v138, -v0
	v_xor_b32_e32 v3, 1, v225
	v_add_u32_e32 v8, 64, v5
	v_mul_f32_e32 v6, v72, v72
	v_cmp_lt_i32_e32 vcc, v3, v8
	v_fmac_f32_e32 v6, v129, v129
	v_fmac_f32_e32 v6, v42, v42
	v_cndmask_b32_e32 v3, v225, v3, vcc
	v_lshlrev_b32_e32 v3, 2, v3
	v_fmac_f32_e32 v6, v25, v25
	ds_bpermute_b32 v7, v3, v6
	v_xor_b32_e32 v5, 2, v225
	v_cmp_lt_i32_e32 vcc, v5, v8
	v_mul_f32_e32 v0, v57, v155
	v_fma_f32 v54, v9, v139, -v0
	v_cndmask_b32_e32 v5, v225, v5, vcc
	v_lshlrev_b32_e32 v5, 2, v5
	s_waitcnt lgkmcnt(0)
	v_add_f32_e32 v7, v6, v7
	ds_bpermute_b32 v9, v5, v7
	v_xor_b32_e32 v6, 4, v225
	v_cmp_lt_i32_e32 vcc, v6, v8
	v_mul_f32_e32 v16, v93, v159
	v_mul_f32_e32 v0, v58, v156
	v_cndmask_b32_e32 v6, v225, v6, vcc
	v_lshlrev_b32_e32 v6, 2, v6
	s_waitcnt lgkmcnt(0)
	v_add_f32_e32 v9, v7, v9
	v_fma_f32 v16, v29, v143, -v16
	v_fma_f32 v29, v10, v140, -v0
	ds_bpermute_b32 v10, v6, v9
	v_xor_b32_e32 v7, 8, v225
	v_cmp_lt_i32_e32 vcc, v7, v8
	v_mul_f32_e32 v0, v59, v157
	v_fma_f32 v23, v11, v141, -v0
	v_cndmask_b32_e32 v7, v225, v7, vcc
	v_lshlrev_b32_e32 v7, 2, v7
	s_waitcnt lgkmcnt(0)
	v_add_f32_e32 v9, v9, v10
	ds_bpermute_b32 v10, v7, v9
	v_xor_b32_e32 v11, 16, v225
	v_mul_f32_e32 v0, v60, v158
	v_cmp_lt_i32_e32 vcc, v11, v8
	v_fma_f32 v4, v12, v142, -v0
	v_mul_f32_e32 v12, v73, v73
	v_cndmask_b32_e32 v8, v225, v11, vcc
	v_lshlrev_b32_e32 v8, 2, v8
	s_waitcnt lgkmcnt(0)
	v_add_f32_e32 v9, v9, v10
	v_fmac_f32_e32 v12, v113, v113
	ds_bpermute_b32 v10, v8, v9
	v_fmac_f32_e32 v12, v43, v43
	v_mul_f32_e32 v0, v61, v159
	v_fmac_f32_e32 v12, v30, v30
	v_fma_f32 v2, v13, v143, -v0
	ds_bpermute_b32 v13, v3, v12
	s_waitcnt lgkmcnt(1)
	v_add_f32_e32 v9, v9, v10
	v_fmamk_f32 v9, v9, 0x3c000000, v222
	s_waitcnt vmcnt(3)
	v_mul_f32_e32 v11, v233, v24
	v_rsq_f32_e32 v24, v9
	s_waitcnt lgkmcnt(0)
	v_add_f32_e32 v9, v12, v13
	ds_bpermute_b32 v10, v5, v9
	v_mul_f32_e32 v0, v62, v160
	v_fma_f32 v1, v14, v144, -v0
	s_waitcnt vmcnt(2)
	v_mul_f32_e32 v14, v233, v26
	s_waitcnt vmcnt(1)
	v_mul_f32_e32 v13, v233, v27
	s_waitcnt lgkmcnt(0)
	v_add_f32_e32 v26, v9, v10
	ds_bpermute_b32 v27, v6, v26
	s_waitcnt vmcnt(0)
	v_mul_f32_e32 v12, v233, v28
	v_mul_f32_e32 v28, v74, v74
	v_fmac_f32_e32 v28, v114, v114
	v_fmac_f32_e32 v28, v44, v44
	v_mul_f32_e32 v18, v95, v161
	s_waitcnt lgkmcnt(0)
	v_add_f32_e32 v26, v26, v27
	v_fmac_f32_e32 v28, v45, v45
	v_fma_f32 v18, v31, v145, -v18
	ds_bpermute_b32 v27, v7, v26
	ds_bpermute_b32 v31, v3, v28
	v_mul_f32_e32 v0, v63, v161
	v_fma_f32 v0, v15, v145, -v0
	v_mul_f32_e32 v15, v11, v24
	s_waitcnt lgkmcnt(1)
	v_add_f32_e32 v26, v26, v27
	s_waitcnt lgkmcnt(0)
	v_add_f32_e32 v28, v28, v31
	ds_bpermute_b32 v27, v8, v26
	ds_bpermute_b32 v31, v5, v28
	v_mul_f32_e32 v10, v129, v15
	v_mul_f32_e32 v15, v13, v24
	v_mul_f32_e32 v15, v42, v15
	s_waitcnt lgkmcnt(1)
	v_add_f32_e32 v26, v26, v27
	s_waitcnt lgkmcnt(0)
	v_add_f32_e32 v27, v28, v31
	ds_bpermute_b32 v28, v6, v27
	v_mul_f32_e32 v31, v75, v75
	v_fmac_f32_e32 v31, v115, v115
	v_fmac_f32_e32 v31, v47, v47
	v_fmac_f32_e32 v31, v48, v48
	s_waitcnt lgkmcnt(0)
	v_add_f32_e32 v27, v27, v28
	ds_bpermute_b32 v28, v7, v27
	v_fmamk_f32 v26, v26, 0x3c000000, v222
	ds_bpermute_b32 v46, v3, v31
	v_rsq_f32_e32 v42, v26
	v_mul_f32_e32 v9, v14, v24
	s_waitcnt lgkmcnt(1)
	v_add_f32_e32 v28, v27, v28
	ds_bpermute_b32 v56, v8, v28
	v_mul_f32_e32 v55, v13, v42
	s_waitcnt lgkmcnt(1)
	v_add_f32_e32 v31, v31, v46
	v_mul_f32_e32 v27, v43, v55
	ds_bpermute_b32 v43, v5, v31
	s_waitcnt lgkmcnt(1)
	v_add_f32_e32 v28, v28, v56
	v_mul_f32_e32 v56, v76, v76
	v_fmac_f32_e32 v56, v116, v116
	v_fmac_f32_e32 v56, v80, v80
	s_waitcnt lgkmcnt(0)
	v_add_f32_e32 v31, v31, v43
	ds_bpermute_b32 v43, v6, v31
	v_fmac_f32_e32 v56, v49, v49
	ds_bpermute_b32 v57, v3, v56
	v_fmamk_f32 v28, v28, 0x3c000000, v222
	v_rsq_f32_e32 v46, v28
	s_waitcnt lgkmcnt(1)
	v_add_f32_e32 v43, v31, v43
	ds_bpermute_b32 v55, v7, v43
	s_waitcnt lgkmcnt(1)
	v_add_f32_e32 v56, v56, v57
	v_mul_f32_e32 v24, v12, v24
	ds_bpermute_b32 v57, v5, v56
	v_mul_f32_e32 v26, v25, v24
	v_mul_f32_e32 v24, v11, v42
	v_mul_f32_e32 v25, v113, v24
	v_mul_f32_e32 v24, v14, v42
	v_mul_f32_e32 v42, v12, v42
	v_mul_f32_e32 v30, v30, v42
	v_mul_f32_e32 v42, v14, v46
	s_waitcnt lgkmcnt(1)
	v_add_f32_e32 v43, v43, v55
	v_mul_f32_e32 v31, v74, v42
	ds_bpermute_b32 v55, v8, v43
	v_mul_f32_e32 v42, v13, v46
	v_mul_f32_e32 v42, v44, v42
	s_waitcnt lgkmcnt(1)
	v_add_f32_e32 v44, v56, v57
	ds_bpermute_b32 v56, v6, v44
	s_waitcnt lgkmcnt(1)
	v_add_f32_e32 v43, v43, v55
	v_fmamk_f32 v43, v43, 0x3c000000, v222
	v_rsq_f32_e32 v55, v43
	v_mul_f32_e32 v43, v12, v46
	s_waitcnt lgkmcnt(0)
	v_add_f32_e32 v56, v44, v56
	ds_bpermute_b32 v57, v7, v56
	v_mul_f32_e32 v44, v14, v55
	v_mul_f32_e32 v28, v11, v46
	v_mul_f32_e32 v46, v45, v43
	v_mul_f32_e32 v45, v75, v44
	v_mul_f32_e32 v44, v13, v55
	v_mul_f32_e32 v44, v47, v44
	s_waitcnt lgkmcnt(0)
	v_add_f32_e32 v47, v56, v57
	v_mul_f32_e32 v57, v77, v77
	v_fmac_f32_e32 v57, v117, v117
	v_fmac_f32_e32 v57, v81, v81
	v_fmac_f32_e32 v57, v50, v50
	ds_bpermute_b32 v56, v8, v47
	ds_bpermute_b32 v58, v3, v57
	v_mul_f32_e32 v59, v78, v78
	v_fmac_f32_e32 v59, v118, v118
	v_fmac_f32_e32 v59, v82, v82
	s_waitcnt lgkmcnt(1)
	v_add_f32_e32 v47, v47, v56
	s_waitcnt lgkmcnt(0)
	v_add_f32_e32 v56, v57, v58
	ds_bpermute_b32 v57, v5, v56
	v_fmac_f32_e32 v59, v51, v51
	ds_bpermute_b32 v60, v3, v59
	v_fmamk_f32 v47, v47, 0x3c000000, v222
	v_rsq_f32_e32 v47, v47
	s_waitcnt lgkmcnt(1)
	v_add_f32_e32 v56, v56, v57
	ds_bpermute_b32 v57, v6, v56
	s_waitcnt lgkmcnt(1)
	v_add_f32_e32 v59, v59, v60
	ds_bpermute_b32 v60, v5, v59
	v_mul_f32_e32 v43, v11, v55
	v_mul_f32_e32 v55, v12, v55
	s_waitcnt lgkmcnt(1)
	v_add_f32_e32 v56, v56, v57
	ds_bpermute_b32 v57, v7, v56
	s_waitcnt lgkmcnt(1)
	v_add_f32_e32 v59, v59, v60
	ds_bpermute_b32 v60, v6, v59
	v_mul_f32_e32 v48, v48, v55
	v_mul_f32_e32 v55, v11, v47
	s_waitcnt lgkmcnt(1)
	v_add_f32_e32 v56, v56, v57
	ds_bpermute_b32 v57, v8, v56
	v_mul_f32_e32 v58, v14, v47
	v_mul_f32_e32 v61, v13, v47
	v_mul_f32_e32 v47, v12, v47
	v_mul_f32_e32 v47, v49, v47
	s_waitcnt lgkmcnt(1)
	v_add_f32_e32 v49, v59, v60
	s_waitcnt lgkmcnt(0)
	v_add_f32_e32 v56, v56, v57
	ds_bpermute_b32 v57, v7, v49
	v_mul_f32_e32 v62, v79, v79
	v_fmac_f32_e32 v62, v112, v112
	v_fmac_f32_e32 v62, v83, v83
	v_fmac_f32_e32 v62, v52, v52
	s_waitcnt lgkmcnt(0)
	v_add_f32_e32 v49, v49, v57
	ds_bpermute_b32 v57, v8, v49
	ds_bpermute_b32 v63, v3, v62
	v_mul_f32_e32 v74, v39, v39
	v_fmac_f32_e32 v74, v71, v71
	v_fmac_f32_e32 v74, v41, v41
	s_waitcnt lgkmcnt(1)
	v_add_f32_e32 v49, v49, v57
	s_waitcnt lgkmcnt(0)
	v_add_f32_e32 v57, v62, v63
	ds_bpermute_b32 v62, v5, v57
	v_fmac_f32_e32 v74, v53, v53
	ds_bpermute_b32 v75, v3, v74
	v_fmamk_f32 v56, v56, 0x3c000000, v222
	v_rsq_f32_e32 v56, v56
	s_waitcnt lgkmcnt(1)
	v_add_f32_e32 v57, v57, v62
	ds_bpermute_b32 v62, v6, v57
	v_fmamk_f32 v49, v49, 0x3c000000, v222
	s_waitcnt lgkmcnt(1)
	v_add_f32_e32 v74, v74, v75
	v_rsq_f32_e32 v49, v49
	ds_bpermute_b32 v75, v5, v74
	s_waitcnt lgkmcnt(1)
	v_add_f32_e32 v57, v57, v62
	ds_bpermute_b32 v62, v7, v57
	v_mul_f32_e32 v9, v72, v9
	v_mul_f32_e32 v59, v11, v56
	v_mul_f32_e32 v60, v14, v56
	v_mul_f32_e32 v72, v13, v56
	s_waitcnt lgkmcnt(0)
	v_add_f32_e32 v57, v57, v62
	ds_bpermute_b32 v62, v8, v57
	v_mul_f32_e32 v56, v12, v56
	v_mul_f32_e32 v24, v73, v24
	v_mul_f32_e32 v63, v81, v72
	v_mul_f32_e32 v50, v50, v56
	v_mul_f32_e32 v56, v11, v49
	v_mul_f32_e32 v72, v14, v49
	v_mul_f32_e32 v73, v13, v49
	v_mul_f32_e32 v49, v12, v49
	v_mul_f32_e32 v49, v51, v49
	v_add_f32_e32 v51, v74, v75
	s_waitcnt lgkmcnt(0)
	v_add_f32_e32 v57, v57, v62
	ds_bpermute_b32 v62, v6, v51
	v_mul_f32_e32 v58, v76, v58
	v_mul_f32_e32 v76, v38, v38
	v_fmac_f32_e32 v76, v70, v70
	v_fmac_f32_e32 v76, v40, v40
	s_waitcnt lgkmcnt(0)
	v_add_f32_e32 v51, v51, v62
	v_fmac_f32_e32 v76, v54, v54
	v_mul_f32_e32 v60, v77, v60
	ds_bpermute_b32 v62, v7, v51
	ds_bpermute_b32 v77, v3, v76
	v_fmamk_f32 v57, v57, 0x3c000000, v222
	v_rsq_f32_e32 v57, v57
	v_mul_f32_e32 v72, v78, v72
	s_waitcnt lgkmcnt(1)
	v_add_f32_e32 v51, v51, v62
	s_waitcnt lgkmcnt(0)
	v_add_f32_e32 v76, v76, v77
	ds_bpermute_b32 v62, v8, v51
	ds_bpermute_b32 v77, v5, v76
	v_mul_f32_e32 v75, v14, v57
	v_mul_f32_e32 v75, v79, v75
	v_mul_f32_e32 v74, v11, v57
	s_waitcnt lgkmcnt(1)
	v_add_f32_e32 v51, v51, v62
	s_waitcnt lgkmcnt(0)
	v_add_f32_e32 v62, v76, v77
	ds_bpermute_b32 v76, v6, v62
	v_mul_f32_e32 v77, v37, v37
	v_fmac_f32_e32 v77, v69, v69
	v_fmamk_f32 v51, v51, 0x3c000000, v222
	v_fmac_f32_e32 v77, v22, v22
	s_waitcnt lgkmcnt(0)
	v_add_f32_e32 v62, v62, v76
	v_rsq_f32_e32 v51, v51
	ds_bpermute_b32 v76, v7, v62
	v_fmac_f32_e32 v77, v29, v29
	ds_bpermute_b32 v79, v3, v77
	v_mul_f32_e32 v78, v13, v57
	v_mul_f32_e32 v57, v12, v57
	v_mul_f32_e32 v52, v52, v57
	v_mul_f32_e32 v57, v11, v51
	v_mul_f32_e32 v57, v71, v57
	v_mul_f32_e32 v71, v14, v51
	s_waitcnt lgkmcnt(1)
	v_add_f32_e32 v62, v62, v76
	v_mul_f32_e32 v39, v39, v71
	ds_bpermute_b32 v71, v8, v62
	s_waitcnt lgkmcnt(1)
	v_add_f32_e32 v77, v77, v79
	ds_bpermute_b32 v79, v5, v77
	v_mul_f32_e32 v76, v13, v51
	v_mul_f32_e32 v41, v41, v76
	s_waitcnt lgkmcnt(1)
	v_add_f32_e32 v62, v62, v71
	v_fmamk_f32 v62, v62, 0x3c000000, v222
	s_waitcnt lgkmcnt(0)
	v_add_f32_e32 v71, v77, v79
	v_rsq_f32_e32 v62, v62
	ds_bpermute_b32 v76, v6, v71
	v_mul_f32_e32 v51, v12, v51
	v_mul_f32_e32 v51, v53, v51
	v_mul_f32_e32 v53, v11, v62
	v_mul_f32_e32 v53, v70, v53
	s_waitcnt lgkmcnt(0)
	v_add_f32_e32 v70, v71, v76
	ds_bpermute_b32 v71, v7, v70
	v_mul_f32_e32 v76, v14, v62
	v_mul_f32_e32 v38, v38, v76
	v_mul_f32_e32 v76, v13, v62
	v_mul_f32_e32 v40, v40, v76
	v_mul_f32_e32 v76, v36, v36
	v_fmac_f32_e32 v76, v68, v68
	v_fmac_f32_e32 v76, v21, v21
	s_waitcnt lgkmcnt(0)
	v_add_f32_e32 v70, v70, v71
	v_fmac_f32_e32 v76, v23, v23
	ds_bpermute_b32 v71, v8, v70
	ds_bpermute_b32 v77, v3, v76
	v_mul_f32_e32 v62, v12, v62
	v_mul_f32_e32 v54, v54, v62
	v_lshlrev_b32_e32 v208, 1, v17
	s_waitcnt lgkmcnt(1)
	v_add_f32_e32 v70, v70, v71
	s_waitcnt lgkmcnt(0)
	v_add_f32_e32 v71, v76, v77
	ds_bpermute_b32 v76, v5, v71
	v_mul_f32_e32 v77, v35, v35
	v_fmac_f32_e32 v77, v67, v67
	v_fmac_f32_e32 v77, v20, v20
	v_fmac_f32_e32 v77, v4, v4
	s_waitcnt lgkmcnt(0)
	v_add_f32_e32 v71, v71, v76
	ds_bpermute_b32 v76, v6, v71
	ds_bpermute_b32 v79, v3, v77
	v_fmamk_f32 v70, v70, 0x3c000000, v222
	v_rsq_f32_e32 v70, v70
	v_bfe_u32 v17, v10, 16, 1
	s_waitcnt lgkmcnt(1)
	v_add_f32_e32 v71, v71, v76
	ds_bpermute_b32 v76, v7, v71
	s_waitcnt lgkmcnt(1)
	v_add_f32_e32 v77, v77, v79
	ds_bpermute_b32 v79, v5, v77
	v_mul_f32_e32 v62, v11, v70
	v_mul_f32_e32 v62, v69, v62
	s_waitcnt lgkmcnt(1)
	v_add_f32_e32 v71, v71, v76
	ds_bpermute_b32 v76, v8, v71
	v_mul_f32_e32 v69, v14, v70
	v_mul_f32_e32 v37, v37, v69
	v_mul_f32_e32 v69, v13, v70
	v_mul_f32_e32 v22, v22, v69
	v_mul_f32_e32 v69, v12, v70
	s_waitcnt lgkmcnt(1)
	v_add_f32_e32 v70, v77, v79
	ds_bpermute_b32 v77, v6, v70
	s_waitcnt lgkmcnt(1)
	v_add_f32_e32 v71, v71, v76
	v_fmamk_f32 v71, v71, 0x3c000000, v222
	v_rsq_f32_e32 v71, v71
	v_mul_f32_e32 v29, v29, v69
	s_waitcnt lgkmcnt(0)
	v_add_f32_e32 v69, v70, v77
	ds_bpermute_b32 v70, v7, v69
	v_mul_f32_e32 v76, v11, v71
	v_mul_f32_e32 v68, v68, v76
	v_mul_f32_e32 v76, v14, v71
	v_mul_f32_e32 v36, v36, v76
	v_mul_f32_e32 v76, v34, v34
	v_fmac_f32_e32 v76, v66, v66
	v_fmac_f32_e32 v76, v16, v16
	s_waitcnt lgkmcnt(0)
	v_add_f32_e32 v69, v69, v70
	v_fmac_f32_e32 v76, v2, v2
	ds_bpermute_b32 v70, v8, v69
	ds_bpermute_b32 v77, v3, v76
	v_mul_f32_e32 v79, v13, v71
	v_mul_f32_e32 v21, v21, v79
	v_mul_f32_e32 v71, v12, v71
	s_waitcnt lgkmcnt(1)
	v_add_f32_e32 v69, v69, v70
	s_waitcnt lgkmcnt(0)
	v_add_f32_e32 v70, v76, v77
	ds_bpermute_b32 v76, v5, v70
	v_mul_f32_e32 v77, v33, v33
	v_fmac_f32_e32 v77, v65, v65
	v_fmamk_f32 v69, v69, 0x3c000000, v222
	v_fmac_f32_e32 v77, v19, v19
	s_waitcnt lgkmcnt(0)
	v_add_f32_e32 v70, v70, v76
	ds_bpermute_b32 v76, v6, v70
	v_rsq_f32_e32 v69, v69
	v_fmac_f32_e32 v77, v1, v1
	ds_bpermute_b32 v79, v3, v77
	v_mul_f32_e32 v23, v23, v71
	s_waitcnt lgkmcnt(1)
	v_add_f32_e32 v70, v70, v76
	ds_bpermute_b32 v76, v7, v70
	v_mul_f32_e32 v71, v11, v69
	v_mul_f32_e32 v67, v67, v71
	v_mul_f32_e32 v71, v14, v69
	v_mul_f32_e32 v35, v35, v71
	v_mul_f32_e32 v71, v13, v69
	s_waitcnt lgkmcnt(0)
	v_add_f32_e32 v70, v70, v76
	v_add_f32_e32 v76, v77, v79
	v_mul_f32_e32 v20, v20, v71
	ds_bpermute_b32 v71, v8, v70
	ds_bpermute_b32 v77, v5, v76
	v_mul_f32_e32 v69, v12, v69
	v_mul_f32_e32 v4, v4, v69
	v_add3_u32 v10, v10, v17, s63
	s_waitcnt lgkmcnt(1)
	v_add_f32_e32 v69, v70, v71
	s_waitcnt lgkmcnt(0)
	v_add_f32_e32 v70, v76, v77
	v_mul_f32_e32 v76, v32, v32
	v_fmac_f32_e32 v76, v64, v64
	v_fmac_f32_e32 v76, v18, v18
	v_fmac_f32_e32 v76, v0, v0
	ds_bpermute_b32 v3, v3, v76
	ds_bpermute_b32 v71, v6, v70
	v_fmamk_f32 v69, v69, 0x3c000000, v222
	v_rsq_f32_e32 v69, v69
	v_mul_f32_e32 v28, v114, v28
	s_waitcnt lgkmcnt(1)
	v_add_f32_e32 v3, v76, v3
	ds_bpermute_b32 v5, v5, v3
	s_waitcnt lgkmcnt(1)
	v_add_f32_e32 v70, v70, v71
	ds_bpermute_b32 v71, v7, v70
	v_mul_f32_e32 v77, v11, v69
	v_mul_f32_e32 v76, v14, v69
	s_waitcnt lgkmcnt(1)
	v_add_f32_e32 v3, v3, v5
	ds_bpermute_b32 v5, v6, v3
	s_waitcnt lgkmcnt(1)
	v_add_f32_e32 v70, v70, v71
	ds_bpermute_b32 v71, v8, v70
	v_mul_f32_e32 v6, v13, v69
	v_mul_f32_e32 v6, v16, v6
	s_waitcnt lgkmcnt(1)
	v_add_f32_e32 v3, v3, v5
	ds_bpermute_b32 v5, v7, v3
	s_waitcnt lgkmcnt(1)
	v_add_f32_e32 v70, v70, v71
	v_fmamk_f32 v70, v70, 0x3c000000, v222
	v_rsq_f32_e32 v70, v70
	v_mul_f32_e32 v7, v12, v69
	s_waitcnt lgkmcnt(0)
	v_add_f32_e32 v3, v3, v5
	ds_bpermute_b32 v5, v8, v3
	v_mul_f32_e32 v7, v2, v7
	v_mul_f32_e32 v2, v11, v70
	v_mul_f32_e32 v8, v65, v2
	v_mul_f32_e32 v2, v14, v70
	s_waitcnt lgkmcnt(0)
	v_add_f32_e32 v3, v3, v5
	v_fmamk_f32 v3, v3, 0x3c000000, v222
	v_rsq_f32_e32 v3, v3
	v_mul_f32_e32 v16, v33, v2
	v_mul_f32_e32 v2, v13, v70
	v_mul_f32_e32 v5, v19, v2
	v_mul_f32_e32 v2, v12, v70
	v_mul_f32_e32 v19, v1, v2
	v_mul_f32_e32 v1, v11, v3
	v_mul_f32_e32 v11, v64, v1
	v_mul_f32_e32 v1, v14, v3
	v_mul_f32_e32 v14, v32, v1
	v_mul_f32_e32 v1, v13, v3
	v_mul_f32_e32 v13, v18, v1
	v_mul_f32_e32 v1, v12, v3
	v_mul_f32_e32 v12, v0, v1
	v_lshl_add_u32 v18, v128, 2, s38
	v_lshl_add_u64 v[0:1], s[14:15], 0, v[208:209]
	v_mad_i64_i32 v[2:3], s[14:15], v18, s62, v[0:1]
	global_store_short_d16_hi v[2:3], v10, off
	v_bfe_u32 v10, v9, 16, 1
	v_add3_u32 v9, v9, v10, s63
	global_store_short_d16_hi v[2:3], v9, off offset:64
	v_bfe_u32 v9, v15, 16, 1
	v_add3_u32 v9, v15, v9, s63
	global_store_short_d16_hi v[2:3], v9, off offset:128
	v_bfe_u32 v9, v26, 16, 1
	v_add3_u32 v9, v26, v9, s63
	global_store_short_d16_hi v[2:3], v9, off offset:192
	v_or_b32_e32 v2, 1, v18
	v_bfe_u32 v9, v25, 16, 1
	v_mad_i64_i32 v[2:3], s[14:15], v2, s62, v[0:1]
	v_add3_u32 v9, v25, v9, s63
	global_store_short_d16_hi v[2:3], v9, off
	v_bfe_u32 v9, v24, 16, 1
	v_add3_u32 v9, v24, v9, s63
	global_store_short_d16_hi v[2:3], v9, off offset:64
	v_bfe_u32 v9, v27, 16, 1
	v_add3_u32 v9, v27, v9, s63
	global_store_short_d16_hi v[2:3], v9, off offset:128
	v_bfe_u32 v9, v30, 16, 1
	v_add3_u32 v9, v30, v9, s63
	global_store_short_d16_hi v[2:3], v9, off offset:192
	v_or_b32_e32 v2, 2, v18
	v_bfe_u32 v9, v28, 16, 1
	v_mad_i64_i32 v[2:3], s[14:15], v2, s62, v[0:1]
	v_add3_u32 v9, v28, v9, s63
	global_store_short_d16_hi v[2:3], v9, off
	v_bfe_u32 v9, v31, 16, 1
	v_add3_u32 v9, v31, v9, s63
	global_store_short_d16_hi v[2:3], v9, off offset:64
	v_bfe_u32 v9, v42, 16, 1
	v_add3_u32 v9, v42, v9, s63
	global_store_short_d16_hi v[2:3], v9, off offset:128
	v_bfe_u32 v9, v46, 16, 1
	v_mul_f32_e32 v43, v115, v43
	v_add3_u32 v9, v46, v9, s63
	global_store_short_d16_hi v[2:3], v9, off offset:192
	v_or_b32_e32 v2, 3, v18
	v_bfe_u32 v9, v43, 16, 1
	v_mad_i64_i32 v[2:3], s[14:15], v2, s62, v[0:1]
	v_add3_u32 v9, v43, v9, s63
	global_store_short_d16_hi v[2:3], v9, off
	v_bfe_u32 v9, v45, 16, 1
	v_add3_u32 v9, v45, v9, s63
	global_store_short_d16_hi v[2:3], v9, off offset:64
	v_bfe_u32 v9, v44, 16, 1
	v_add3_u32 v9, v44, v9, s63
	global_store_short_d16_hi v[2:3], v9, off offset:128
	v_bfe_u32 v9, v48, 16, 1
	v_mul_f32_e32 v55, v116, v55
	v_add3_u32 v9, v48, v9, s63
	global_store_short_d16_hi v[2:3], v9, off offset:192
	v_add_u32_e32 v2, 8, v18
	v_bfe_u32 v9, v55, 16, 1
	v_mad_i64_i32 v[2:3], s[14:15], v2, s62, v[0:1]
	v_add3_u32 v9, v55, v9, s63
	global_store_short_d16_hi v[2:3], v9, off
	v_bfe_u32 v9, v58, 16, 1
	v_mul_f32_e32 v61, v80, v61
	v_add3_u32 v9, v58, v9, s63
	global_store_short_d16_hi v[2:3], v9, off offset:64
	v_bfe_u32 v9, v61, 16, 1
	v_add3_u32 v9, v61, v9, s63
	global_store_short_d16_hi v[2:3], v9, off offset:128
	v_bfe_u32 v9, v47, 16, 1
	v_mul_f32_e32 v59, v117, v59
	v_add3_u32 v9, v47, v9, s63
	global_store_short_d16_hi v[2:3], v9, off offset:192
	v_add_u32_e32 v2, 9, v18
	v_bfe_u32 v9, v59, 16, 1
	v_mad_i64_i32 v[2:3], s[14:15], v2, s62, v[0:1]
	v_add3_u32 v9, v59, v9, s63
	global_store_short_d16_hi v[2:3], v9, off
	v_bfe_u32 v9, v60, 16, 1
	v_add3_u32 v9, v60, v9, s63
	global_store_short_d16_hi v[2:3], v9, off offset:64
	v_bfe_u32 v9, v63, 16, 1
	v_add3_u32 v9, v63, v9, s63
	global_store_short_d16_hi v[2:3], v9, off offset:128
	v_bfe_u32 v9, v50, 16, 1
	v_mul_f32_e32 v56, v118, v56
	v_add3_u32 v9, v50, v9, s63
	global_store_short_d16_hi v[2:3], v9, off offset:192
	v_add_u32_e32 v2, 10, v18
	v_bfe_u32 v9, v56, 16, 1
	v_mad_i64_i32 v[2:3], s[14:15], v2, s62, v[0:1]
	v_add3_u32 v9, v56, v9, s63
	global_store_short_d16_hi v[2:3], v9, off
	v_bfe_u32 v9, v72, 16, 1
	v_mul_f32_e32 v73, v82, v73
	v_add3_u32 v9, v72, v9, s63
	global_store_short_d16_hi v[2:3], v9, off offset:64
	v_bfe_u32 v9, v73, 16, 1
	v_add3_u32 v9, v73, v9, s63
	global_store_short_d16_hi v[2:3], v9, off offset:128
	v_bfe_u32 v9, v49, 16, 1
	v_mul_f32_e32 v74, v112, v74
	v_add3_u32 v9, v49, v9, s63
	global_store_short_d16_hi v[2:3], v9, off offset:192
	v_add_u32_e32 v2, 11, v18
	v_bfe_u32 v9, v74, 16, 1
	v_mad_i64_i32 v[2:3], s[14:15], v2, s62, v[0:1]
	v_add3_u32 v9, v74, v9, s63
	global_store_short_d16_hi v[2:3], v9, off
	v_bfe_u32 v9, v75, 16, 1
	v_mul_f32_e32 v78, v83, v78
	v_add3_u32 v9, v75, v9, s63
	global_store_short_d16_hi v[2:3], v9, off offset:64
	v_bfe_u32 v9, v78, 16, 1
	v_add3_u32 v9, v78, v9, s63
	global_store_short_d16_hi v[2:3], v9, off offset:128
	v_bfe_u32 v9, v52, 16, 1
	v_add3_u32 v9, v52, v9, s63
	global_store_short_d16_hi v[2:3], v9, off offset:192
	v_add_u32_e32 v2, 16, v18
	v_bfe_u32 v9, v57, 16, 1
	v_mad_i64_i32 v[2:3], s[14:15], v2, s62, v[0:1]
	v_add3_u32 v9, v57, v9, s63
	global_store_short_d16_hi v[2:3], v9, off
	v_bfe_u32 v9, v39, 16, 1
	v_add3_u32 v9, v39, v9, s63
	global_store_short_d16_hi v[2:3], v9, off offset:64
	v_bfe_u32 v9, v41, 16, 1
	v_add3_u32 v9, v41, v9, s63
	global_store_short_d16_hi v[2:3], v9, off offset:128
	v_bfe_u32 v9, v51, 16, 1
	v_add3_u32 v9, v51, v9, s63
	global_store_short_d16_hi v[2:3], v9, off offset:192
	v_add_u32_e32 v2, 17, v18
	v_bfe_u32 v9, v53, 16, 1
	v_mad_i64_i32 v[2:3], s[14:15], v2, s62, v[0:1]
	v_add3_u32 v9, v53, v9, s63
	global_store_short_d16_hi v[2:3], v9, off
	v_bfe_u32 v9, v38, 16, 1
	v_add3_u32 v9, v38, v9, s63
	global_store_short_d16_hi v[2:3], v9, off offset:64
	v_bfe_u32 v9, v40, 16, 1
	v_add3_u32 v9, v40, v9, s63
	global_store_short_d16_hi v[2:3], v9, off offset:128
	v_bfe_u32 v9, v54, 16, 1
	v_add3_u32 v9, v54, v9, s63
	global_store_short_d16_hi v[2:3], v9, off offset:192
	v_add_u32_e32 v2, 18, v18
	v_bfe_u32 v9, v62, 16, 1
	v_mad_i64_i32 v[2:3], s[14:15], v2, s62, v[0:1]
	v_add3_u32 v9, v62, v9, s63
	global_store_short_d16_hi v[2:3], v9, off
	v_bfe_u32 v9, v37, 16, 1
	v_add3_u32 v9, v37, v9, s63
	global_store_short_d16_hi v[2:3], v9, off offset:64
	v_bfe_u32 v9, v22, 16, 1
	v_add3_u32 v9, v22, v9, s63
	global_store_short_d16_hi v[2:3], v9, off offset:128
	v_bfe_u32 v9, v29, 16, 1
	v_add3_u32 v9, v29, v9, s63
	global_store_short_d16_hi v[2:3], v9, off offset:192
	v_add_u32_e32 v2, 19, v18
	v_bfe_u32 v9, v68, 16, 1
	v_mad_i64_i32 v[2:3], s[14:15], v2, s62, v[0:1]
	v_add3_u32 v9, v68, v9, s63
	global_store_short_d16_hi v[2:3], v9, off
	v_bfe_u32 v9, v36, 16, 1
	v_add3_u32 v9, v36, v9, s63
	global_store_short_d16_hi v[2:3], v9, off offset:64
	v_bfe_u32 v9, v21, 16, 1
	v_add3_u32 v9, v21, v9, s63
	global_store_short_d16_hi v[2:3], v9, off offset:128
	v_bfe_u32 v9, v23, 16, 1
	v_add3_u32 v9, v23, v9, s63
	global_store_short_d16_hi v[2:3], v9, off offset:192
	v_add_u32_e32 v2, 24, v18
	v_bfe_u32 v9, v67, 16, 1
	v_mad_i64_i32 v[2:3], s[14:15], v2, s62, v[0:1]
	v_add3_u32 v9, v67, v9, s63
	global_store_short_d16_hi v[2:3], v9, off
	v_bfe_u32 v9, v35, 16, 1
	v_add3_u32 v9, v35, v9, s63
	global_store_short_d16_hi v[2:3], v9, off offset:64
	v_bfe_u32 v9, v20, 16, 1
	v_add3_u32 v9, v20, v9, s63
	global_store_short_d16_hi v[2:3], v9, off offset:128
	v_bfe_u32 v9, v4, 16, 1
	v_mul_f32_e32 v66, v66, v77
	v_add3_u32 v4, v4, v9, s63
	global_store_short_d16_hi v[2:3], v4, off offset:192
	v_add_u32_e32 v2, 25, v18
	v_bfe_u32 v4, v66, 16, 1
	v_mul_f32_e32 v34, v34, v76
	v_mad_i64_i32 v[2:3], s[14:15], v2, s62, v[0:1]
	v_add3_u32 v4, v66, v4, s63
	global_store_short_d16_hi v[2:3], v4, off
	v_bfe_u32 v4, v34, 16, 1
	v_add3_u32 v4, v34, v4, s63
	global_store_short_d16_hi v[2:3], v4, off offset:64
	v_bfe_u32 v4, v6, 16, 1
	v_add3_u32 v4, v6, v4, s63
	global_store_short_d16_hi v[2:3], v4, off offset:128
	v_bfe_u32 v4, v7, 16, 1
	v_add3_u32 v4, v7, v4, s63
	global_store_short_d16_hi v[2:3], v4, off offset:192
	v_add_u32_e32 v2, 26, v18
	v_bfe_u32 v4, v8, 16, 1
	v_mad_i64_i32 v[2:3], s[14:15], v2, s62, v[0:1]
	v_add3_u32 v4, v8, v4, s63
	global_store_short_d16_hi v[2:3], v4, off
	v_bfe_u32 v4, v16, 16, 1
	v_add3_u32 v4, v16, v4, s63
	global_store_short_d16_hi v[2:3], v4, off offset:64
	v_bfe_u32 v4, v5, 16, 1
	v_add3_u32 v4, v5, v4, s63
	global_store_short_d16_hi v[2:3], v4, off offset:128
	v_bfe_u32 v4, v19, 16, 1
	v_add3_u32 v4, v19, v4, s63
	global_store_short_d16_hi v[2:3], v4, off offset:192
	v_add_u32_e32 v2, 27, v18
	v_mad_i64_i32 v[0:1], s[14:15], v2, s62, v[0:1]
	v_bfe_u32 v2, v11, 16, 1
	v_add3_u32 v2, v11, v2, s63
	global_store_short_d16_hi v[0:1], v2, off
	v_bfe_u32 v2, v14, 16, 1
	v_add3_u32 v2, v14, v2, s63
	global_store_short_d16_hi v[0:1], v2, off offset:64
	v_bfe_u32 v2, v13, 16, 1
	v_add3_u32 v2, v13, v2, s63
	global_store_short_d16_hi v[0:1], v2, off offset:128
	v_bfe_u32 v2, v12, 16, 1
	v_add3_u32 v2, v12, v2, s63
	s_mov_b64 s[14:15], 0
	s_and_b64 vcc, exec, s[12:13]
	global_store_short_d16_hi v[0:1], v2, off offset:192
	s_waitcnt vmcnt(63) expcnt(7) lgkmcnt(15)
	s_barrier
	s_cbranch_vccnz .LBB0_559

.Lattn_nobias0_a:
	v_max3_f32 v228, v160, v161, v162
	v_max3_f32 v229, v163, v164, v165
	s_waitcnt lgkmcnt(4)
	v_mfma_f32_32x32x16_bf16 v[112:127], v[128:131], v[144:147], v[112:127]
	ds_read_b64_tr_b16 v[156:157], v215 offset:32768
	ds_read_b64_tr_b16 v[158:159], v215 offset:34816
	v_max3_f32 v228, v228, v166, v167
	v_max3_f32 v229, v229, v168, v169
	v_max3_f32 v228, v228, v170, v171
	v_max3_f32 v229, v229, v172, v173
	v_max3_f32 v228, v228, v174, v175
	v_max3_f32 v229, v229, v176, v177
	s_waitcnt lgkmcnt(4)
	v_mfma_f32_32x32x16_bf16 v[96:111], v[128:131], v[148:151], v[96:111]
	ds_read_b64_tr_b16 v[144:145], v212 offset:36864
	ds_read_b64_tr_b16 v[146:147], v212 offset:38912
	v_max3_f32 v228, v228, v178, v179
	v_max3_f32 v229, v229, v180, v181
	v_max3_f32 v228, v228, v182, v183
	v_max3_f32 v229, v229, v184, v185
	v_max3_f32 v228, v228, v186, v187
	v_max3_f32 v229, v229, v188, v189
	s_waitcnt lgkmcnt(4)
	v_mfma_f32_32x32x16_bf16 v[80:95], v[128:131], v[152:155], v[80:95]
	ds_read_b64_tr_b16 v[148:149], v213 offset:36864
	ds_read_b64_tr_b16 v[150:151], v213 offset:38912
	v_max3_f32 v228, v228, v190, v191
	v_max_f32_e32 v228, v228, v229
	v_mov_b32_e32 v229, v228
	s_nop 1
	v_permlane32_swap_b32_e32 v228, v229
	v_max_f32_e32 v228, v228, v229
	v_add_f32_e32 v228, s49, v228
	v_sub_f32_e32 v229, v228, v226
	v_cmp_lt_f32_e32 vcc, 0x41000000, v229
	s_cbranch_vccz .Lattn_noresc0_a
	s_nop 0
	v_cndmask_b32_e32 v229, v226, v228, vcc
	v_sub_f32_e32 v228, v226, v229
	v_exp_f32_e32 v228, v228
	v_mov_b32_e32 v226, v229
	ds_write_b32 v239, v228
	ds_read_b128 v[192:195], v249
	ds_read_b128 v[196:199], v249 offset:32
	ds_read_b128 v[200:203], v249 offset:64
	ds_read_b128 v[204:207], v249 offset:96
	v_mul_f32_e32 v251, v251, v228
	s_waitcnt lgkmcnt(3)
	v_pk_mul_f32 v[64:65], v[64:65], v[192:193]
	v_pk_mul_f32 v[66:67], v[66:67], v[194:195]
	v_pk_mul_f32 v[32:33], v[32:33], v[192:193]
	v_pk_mul_f32 v[34:35], v[34:35], v[194:195]
	v_pk_mul_f32 v[16:17], v[16:17], v[192:193]
	v_pk_mul_f32 v[18:19], v[18:19], v[194:195]
	v_pk_mul_f32 v[0:1], v[0:1], v[192:193]
	v_pk_mul_f32 v[2:3], v[2:3], v[194:195]
	s_waitcnt lgkmcnt(2)
	v_pk_mul_f32 v[68:69], v[68:69], v[196:197]
	v_pk_mul_f32 v[70:71], v[70:71], v[198:199]
	v_pk_mul_f32 v[36:37], v[36:37], v[196:197]
	v_pk_mul_f32 v[38:39], v[38:39], v[198:199]
	v_pk_mul_f32 v[20:21], v[20:21], v[196:197]
	v_pk_mul_f32 v[22:23], v[22:23], v[198:199]
	v_pk_mul_f32 v[4:5], v[4:5], v[196:197]
	v_pk_mul_f32 v[6:7], v[6:7], v[198:199]
	s_waitcnt lgkmcnt(1)
	v_pk_mul_f32 v[72:73], v[72:73], v[200:201]
	v_pk_mul_f32 v[74:75], v[74:75], v[202:203]
	v_pk_mul_f32 v[40:41], v[40:41], v[200:201]
	v_pk_mul_f32 v[42:43], v[42:43], v[202:203]
	v_pk_mul_f32 v[24:25], v[24:25], v[200:201]
	v_pk_mul_f32 v[26:27], v[26:27], v[202:203]
	v_pk_mul_f32 v[8:9], v[8:9], v[200:201]
	v_pk_mul_f32 v[10:11], v[10:11], v[202:203]
	s_waitcnt lgkmcnt(0)
	v_pk_mul_f32 v[76:77], v[76:77], v[204:205]
	v_pk_mul_f32 v[78:79], v[78:79], v[206:207]
	v_pk_mul_f32 v[44:45], v[44:45], v[204:205]
	v_pk_mul_f32 v[46:47], v[46:47], v[206:207]
	v_pk_mul_f32 v[28:29], v[28:29], v[204:205]
	v_pk_mul_f32 v[30:31], v[30:31], v[206:207]
	v_pk_mul_f32 v[12:13], v[12:13], v[204:205]
	v_pk_mul_f32 v[14:15], v[14:15], v[206:207]
.Lattn_noresc0_a:
	v_subrev_f32_e32 v229, s49, v226
	ds_read_b64_tr_b16 v[152:153], v214 offset:36864
	ds_read_b64_tr_b16 v[154:155], v214 offset:38912
	ds_read_b64_tr_b16 v[192:193], v215 offset:36864
	ds_read_b64_tr_b16 v[194:195], v215 offset:38912
	ds_read_b64_tr_b16 v[196:197], v212 offset:40960
	ds_read_b64_tr_b16 v[198:199], v212 offset:43008
	ds_read_b64_tr_b16 v[200:201], v213 offset:40960
	ds_read_b64_tr_b16 v[202:203], v213 offset:43008
	v_sub_f32_e32 v160, v160, v229
	v_sub_f32_e32 v161, v161, v229
	v_sub_f32_e32 v162, v162, v229
	s_waitcnt lgkmcnt(12)
	v_mfma_f32_32x32x16_bf16 v[48:63], v[128:131], v[156:159], v[48:63]
	ds_read_b64_tr_b16 v[204:205], v214 offset:40960
	ds_read_b64_tr_b16 v[206:207], v214 offset:43008
	v_sub_f32_e32 v163, v163, v229
	v_exp_f32_e32 v160, v160
	v_exp_f32_e32 v161, v161
	v_exp_f32_e32 v162, v162
	s_waitcnt lgkmcnt(12)
	v_mfma_f32_32x32x16_bf16 v[112:127], v[132:135], v[144:147], v[112:127]
	ds_read_b64_tr_b16 v[156:157], v215 offset:40960
	ds_read_b64_tr_b16 v[158:159], v215 offset:43008
	v_exp_f32_e32 v163, v163
	v_add_f32_e32 v254, v160, v161
	v_add_f32_e32 v254, v254, v162
	v_add_f32_e32 v254, v254, v163
	v_sub_f32_e32 v164, v164, v229
	s_waitcnt lgkmcnt(12)
	v_mfma_f32_32x32x16_bf16 v[96:111], v[132:135], v[148:151], v[96:111]
	ds_read_b64_tr_b16 v[144:145], v212 offset:45056
	ds_read_b64_tr_b16 v[146:147], v212 offset:47104
	v_sub_f32_e32 v165, v165, v229
	v_sub_f32_e32 v166, v166, v229
	v_sub_f32_e32 v167, v167, v229
	v_exp_f32_e32 v164, v164
	s_waitcnt lgkmcnt(12)
	v_mfma_f32_32x32x16_bf16 v[80:95], v[132:135], v[152:155], v[80:95]
	ds_read_b64_tr_b16 v[148:149], v213 offset:45056
	ds_read_b64_tr_b16 v[150:151], v213 offset:47104
	v_exp_f32_e32 v165, v165
	v_exp_f32_e32 v166, v166
	v_exp_f32_e32 v167, v167
	v_add_f32_e32 v254, v254, v164
	v_add_f32_e32 v254, v254, v165
	s_waitcnt lgkmcnt(12)
	v_mfma_f32_32x32x16_bf16 v[48:63], v[132:135], v[192:195], v[48:63]
	ds_read_b64_tr_b16 v[152:153], v214 offset:45056
	ds_read_b64_tr_b16 v[154:155], v214 offset:47104
	v_add_f32_e32 v254, v254, v166
	v_add_f32_e32 v254, v254, v167
	v_cvt_pk_bf16_f32 v160, v160, v161
	v_cvt_pk_bf16_f32 v161, v162, v163
	v_sub_f32_e32 v168, v168, v229
	s_waitcnt lgkmcnt(12)
	v_mfma_f32_32x32x16_bf16 v[112:127], v[136:139], v[196:199], v[112:127]
	ds_read_b64_tr_b16 v[192:193], v215 offset:45056
	ds_read_b64_tr_b16 v[194:195], v215 offset:47104
	v_sub_f32_e32 v169, v169, v229
	v_sub_f32_e32 v170, v170, v229
	v_sub_f32_e32 v171, v171, v229
	v_exp_f32_e32 v168, v168
	s_waitcnt lgkmcnt(12)
	v_mfma_f32_32x32x16_bf16 v[96:111], v[136:139], v[200:203], v[96:111]
	ds_read_b128 v[196:199], v244
	v_exp_f32_e32 v169, v169
	v_exp_f32_e32 v170, v170
	v_exp_f32_e32 v171, v171
	v_add_f32_e32 v254, v254, v168
	v_add_f32_e32 v254, v254, v169
	s_waitcnt lgkmcnt(11)
	v_mfma_f32_32x32x16_bf16 v[80:95], v[136:139], v[204:207], v[80:95]
	v_add3_u32 v230, v237, v244, s48
	ds_read_b128 v[200:203], v230
	ds_read_b128 v[204:207], v230 offset:8192
	v_add_f32_e32 v254, v254, v170
	v_add_f32_e32 v254, v254, v171
	v_cvt_pk_bf16_f32 v162, v164, v165
	v_cvt_pk_bf16_f32 v163, v166, v167
	v_sub_f32_e32 v172, v172, v229
	s_waitcnt lgkmcnt(11)
	v_mfma_f32_32x32x16_bf16 v[48:63], v[136:139], v[156:159], v[48:63]
	v_sub_f32_e32 v173, v173, v229
	v_sub_f32_e32 v174, v174, v229
	v_sub_f32_e32 v175, v175, v229
	v_exp_f32_e32 v172, v172
	s_waitcnt lgkmcnt(9)
	v_mfma_f32_32x32x16_bf16 v[112:127], v[140:143], v[144:147], v[112:127]
	v_exp_f32_e32 v173, v173
	v_exp_f32_e32 v174, v174
	v_exp_f32_e32 v175, v175
	v_add_f32_e32 v254, v254, v172
	v_add_f32_e32 v254, v254, v173
	s_waitcnt lgkmcnt(7)
	v_mfma_f32_32x32x16_bf16 v[96:111], v[140:143], v[148:151], v[96:111]
	v_add_f32_e32 v254, v254, v174
	v_add_f32_e32 v254, v254, v175
	v_cvt_pk_bf16_f32 v164, v168, v169
	v_cvt_pk_bf16_f32 v165, v170, v171
	v_sub_f32_e32 v176, v176, v229
	s_waitcnt lgkmcnt(5)
	v_mfma_f32_32x32x16_bf16 v[80:95], v[140:143], v[152:155], v[80:95]
	v_sub_f32_e32 v177, v177, v229
	v_sub_f32_e32 v178, v178, v229
	v_sub_f32_e32 v179, v179, v229
	v_exp_f32_e32 v176, v176
	s_waitcnt lgkmcnt(3)
	v_mfma_f32_32x32x16_bf16 v[48:63], v[140:143], v[192:195], v[48:63]
	ds_read_b128 v[192:195], v245
	v_exp_f32_e32 v177, v177
	v_exp_f32_e32 v178, v178
	v_exp_f32_e32 v179, v179
	v_add_f32_e32 v255, v176, v177
	v_add_f32_e32 v255, v255, v178
	s_waitcnt lgkmcnt(2)
	v_mfma_f32_32x32x16_bf16 v[128:143], v[200:203], v[196:199], 0
	v_add_f32_e32 v255, v255, v179
	v_cvt_pk_bf16_f32 v166, v172, v173
	v_cvt_pk_bf16_f32 v167, v174, v175
	v_sub_f32_e32 v180, v180, v229
	v_sub_f32_e32 v181, v181, v229
	s_waitcnt lgkmcnt(1)
	v_mfma_f32_32x32x16_bf16 v[144:159], v[204:207], v[196:199], 0
	v_add3_u32 v230, v237, v245, s48
	ds_read_b128 v[200:203], v230
	ds_read_b128 v[204:207], v230 offset:8192
	ds_read_b128 v[196:199], v246
	v_sub_f32_e32 v182, v182, v229
	v_sub_f32_e32 v183, v183, v229
	v_exp_f32_e32 v180, v180
	v_exp_f32_e32 v181, v181
	s_waitcnt lgkmcnt(2)
	v_mfma_f32_32x32x16_bf16 v[128:143], v[200:203], v[192:195], v[128:143]
	v_exp_f32_e32 v182, v182
	v_exp_f32_e32 v183, v183
	v_add_f32_e32 v255, v255, v180
	v_add_f32_e32 v255, v255, v181
	v_add_f32_e32 v255, v255, v182
	s_waitcnt lgkmcnt(1)
	v_mfma_f32_32x32x16_bf16 v[144:159], v[204:207], v[192:195], v[144:159]
	v_add3_u32 v230, v237, v246, s48
	ds_read_b128 v[200:203], v230
	ds_read_b128 v[204:207], v230 offset:8192
	ds_read_b128 v[192:195], v247
	v_add_f32_e32 v255, v255, v183
	v_cvt_pk_bf16_f32 v168, v176, v177
	v_cvt_pk_bf16_f32 v169, v178, v179
	v_sub_f32_e32 v184, v184, v229
	v_sub_f32_e32 v185, v185, v229
	s_waitcnt lgkmcnt(2)
	v_mfma_f32_32x32x16_bf16 v[128:143], v[200:203], v[196:199], v[128:143]
	v_sub_f32_e32 v186, v186, v229
	v_sub_f32_e32 v187, v187, v229
	v_exp_f32_e32 v184, v184
	v_exp_f32_e32 v185, v185
	s_waitcnt lgkmcnt(1)
	v_mfma_f32_32x32x16_bf16 v[144:159], v[204:207], v[196:199], v[144:159]
	v_add3_u32 v230, v237, v247, s48
	ds_read_b128 v[200:203], v230
	ds_read_b128 v[204:207], v230 offset:8192
	v_exp_f32_e32 v186, v186
	v_exp_f32_e32 v187, v187
	v_add_f32_e32 v255, v255, v184
	v_add_f32_e32 v255, v255, v185
	v_add_f32_e32 v255, v255, v186
	s_waitcnt lgkmcnt(1)
	v_mfma_f32_32x32x16_bf16 v[128:143], v[200:203], v[192:195], v[128:143]
	v_add_f32_e32 v255, v255, v187
	v_cvt_pk_bf16_f32 v170, v180, v181
	v_cvt_pk_bf16_f32 v171, v182, v183
	v_sub_f32_e32 v188, v188, v229
	v_sub_f32_e32 v189, v189, v229
	s_waitcnt lgkmcnt(0)
	v_mfma_f32_32x32x16_bf16 v[144:159], v[204:207], v[192:195], v[144:159]
	v_sub_f32_e32 v190, v190, v229
	v_sub_f32_e32 v191, v191, v229
	v_exp_f32_e32 v188, v188
	v_exp_f32_e32 v189, v189
	v_exp_f32_e32 v190, v190
	v_exp_f32_e32 v191, v191
	v_add_f32_e32 v255, v255, v188
	v_add_f32_e32 v255, v255, v189
	v_add_f32_e32 v255, v255, v190
	v_add_f32_e32 v255, v255, v191
	v_cvt_pk_bf16_f32 v172, v184, v185
	v_cvt_pk_bf16_f32 v173, v186, v187
	v_cvt_pk_bf16_f32 v174, v188, v189
	v_cvt_pk_bf16_f32 v175, v190, v191
	v_add_f32_e32 v254, v254, v255
	v_add_f32_e32 v251, v251, v254
	s_branch .Lattn_mid

.Lattn_nobias0_b:
	v_max3_f32 v228, v160, v161, v162
	v_max3_f32 v229, v163, v164, v165
	v_max3_f32 v228, v228, v166, v167
	v_max3_f32 v229, v229, v168, v169
	v_max3_f32 v228, v228, v170, v171
	v_max3_f32 v229, v229, v172, v173
	v_max3_f32 v228, v228, v174, v175
	v_max3_f32 v229, v229, v176, v177
	v_max3_f32 v228, v228, v178, v179
	v_max3_f32 v229, v229, v180, v181
	v_max3_f32 v228, v228, v182, v183
	v_max3_f32 v229, v229, v184, v185
	v_max3_f32 v228, v228, v186, v187
	v_max3_f32 v229, v229, v188, v189
	v_max3_f32 v228, v228, v190, v191
	v_max_f32_e32 v228, v228, v229
	v_mov_b32_e32 v229, v228
	s_nop 1
	v_permlane32_swap_b32_e32 v228, v229
	v_max_f32_e32 v228, v228, v229
	v_add_f32_e32 v228, s49, v228
	v_sub_f32_e32 v229, v228, v226
	v_cmp_lt_f32_e32 vcc, 0x41000000, v229
	s_cbranch_vccz .Lattn_noresc0_b
	s_nop 0
	v_cndmask_b32_e32 v229, v226, v228, vcc
	v_sub_f32_e32 v228, v226, v229
	v_exp_f32_e32 v228, v228
	v_mov_b32_e32 v226, v229
	ds_write_b32 v239, v228
	ds_read_b128 v[192:195], v249
	ds_read_b128 v[196:199], v249 offset:32
	ds_read_b128 v[200:203], v249 offset:64
	ds_read_b128 v[204:207], v249 offset:96
	v_mul_f32_e32 v251, v251, v228
	s_waitcnt lgkmcnt(3)
	v_pk_mul_f32 v[64:65], v[64:65], v[192:193]
	v_pk_mul_f32 v[66:67], v[66:67], v[194:195]
	v_pk_mul_f32 v[32:33], v[32:33], v[192:193]
	v_pk_mul_f32 v[34:35], v[34:35], v[194:195]
	v_pk_mul_f32 v[16:17], v[16:17], v[192:193]
	v_pk_mul_f32 v[18:19], v[18:19], v[194:195]
	v_pk_mul_f32 v[0:1], v[0:1], v[192:193]
	v_pk_mul_f32 v[2:3], v[2:3], v[194:195]
	s_waitcnt lgkmcnt(2)
	v_pk_mul_f32 v[68:69], v[68:69], v[196:197]
	v_pk_mul_f32 v[70:71], v[70:71], v[198:199]
	v_pk_mul_f32 v[36:37], v[36:37], v[196:197]
	v_pk_mul_f32 v[38:39], v[38:39], v[198:199]
	v_pk_mul_f32 v[20:21], v[20:21], v[196:197]
	v_pk_mul_f32 v[22:23], v[22:23], v[198:199]
	v_pk_mul_f32 v[4:5], v[4:5], v[196:197]
	v_pk_mul_f32 v[6:7], v[6:7], v[198:199]
	s_waitcnt lgkmcnt(1)
	v_pk_mul_f32 v[72:73], v[72:73], v[200:201]
	v_pk_mul_f32 v[74:75], v[74:75], v[202:203]
	v_pk_mul_f32 v[40:41], v[40:41], v[200:201]
	v_pk_mul_f32 v[42:43], v[42:43], v[202:203]
	v_pk_mul_f32 v[24:25], v[24:25], v[200:201]
	v_pk_mul_f32 v[26:27], v[26:27], v[202:203]
	v_pk_mul_f32 v[8:9], v[8:9], v[200:201]
	v_pk_mul_f32 v[10:11], v[10:11], v[202:203]
	s_waitcnt lgkmcnt(0)
	v_pk_mul_f32 v[76:77], v[76:77], v[204:205]
	v_pk_mul_f32 v[78:79], v[78:79], v[206:207]
	v_pk_mul_f32 v[44:45], v[44:45], v[204:205]
	v_pk_mul_f32 v[46:47], v[46:47], v[206:207]
	v_pk_mul_f32 v[28:29], v[28:29], v[204:205]
	v_pk_mul_f32 v[30:31], v[30:31], v[206:207]
	v_pk_mul_f32 v[12:13], v[12:13], v[204:205]
	v_pk_mul_f32 v[14:15], v[14:15], v[206:207]
.Lattn_noresc0_b:
	v_subrev_f32_e32 v229, s49, v226
	ds_read_b128 v[192:195], v244
	v_add3_u32 v230, v237, v244, s48
	ds_read_b128 v[196:199], v230
	ds_read_b128 v[200:203], v230 offset:8192
	ds_read_b128 v[204:207], v245
	v_sub_f32_e32 v160, v160, v229
	v_sub_f32_e32 v161, v161, v229
	v_sub_f32_e32 v162, v162, v229
	s_waitcnt lgkmcnt(2)
	v_mfma_f32_32x32x16_bf16 v[128:143], v[196:199], v[192:195], 0
	v_sub_f32_e32 v163, v163, v229
	v_exp_f32_e32 v160, v160
	v_exp_f32_e32 v161, v161
	v_exp_f32_e32 v162, v162
	v_exp_f32_e32 v163, v163
	v_add_f32_e32 v254, v160, v161
	v_add_f32_e32 v254, v254, v162
	v_add_f32_e32 v254, v254, v163
	v_sub_f32_e32 v164, v164, v229
	v_sub_f32_e32 v165, v165, v229
	v_sub_f32_e32 v166, v166, v229
	v_sub_f32_e32 v167, v167, v229
	v_exp_f32_e32 v164, v164
	s_waitcnt lgkmcnt(1)
	v_mfma_f32_32x32x16_bf16 v[144:159], v[200:203], v[192:195], 0
	v_add3_u32 v230, v237, v245, s48
	ds_read_b128 v[196:199], v230
	ds_read_b128 v[200:203], v230 offset:8192
	ds_read_b128 v[192:195], v246
	v_exp_f32_e32 v165, v165
	v_exp_f32_e32 v166, v166
	v_exp_f32_e32 v167, v167
	v_add_f32_e32 v254, v254, v164
	v_add_f32_e32 v254, v254, v165
	v_add_f32_e32 v254, v254, v166
	v_add_f32_e32 v254, v254, v167
	v_cvt_pk_bf16_f32 v160, v160, v161
	v_cvt_pk_bf16_f32 v161, v162, v163
	v_sub_f32_e32 v168, v168, v229
	v_sub_f32_e32 v169, v169, v229
	v_sub_f32_e32 v170, v170, v229
	v_sub_f32_e32 v171, v171, v229
	s_waitcnt lgkmcnt(2)
	v_mfma_f32_32x32x16_bf16 v[128:143], v[196:199], v[204:207], v[128:143]
	v_exp_f32_e32 v168, v168
	v_exp_f32_e32 v169, v169
	v_exp_f32_e32 v170, v170
	v_exp_f32_e32 v171, v171
	v_add_f32_e32 v254, v254, v168
	v_add_f32_e32 v254, v254, v169
	v_add_f32_e32 v254, v254, v170
	v_add_f32_e32 v254, v254, v171
	v_cvt_pk_bf16_f32 v162, v164, v165
	v_cvt_pk_bf16_f32 v163, v166, v167
	v_sub_f32_e32 v172, v172, v229
	v_sub_f32_e32 v173, v173, v229
	v_sub_f32_e32 v174, v174, v229
	s_waitcnt lgkmcnt(1)
	v_mfma_f32_32x32x16_bf16 v[144:159], v[200:203], v[204:207], v[144:159]
	v_add3_u32 v230, v237, v246, s48
	ds_read_b128 v[196:199], v230
	ds_read_b128 v[200:203], v230 offset:8192
	ds_read_b128 v[204:207], v247
	v_sub_f32_e32 v175, v175, v229
	v_exp_f32_e32 v172, v172
	v_exp_f32_e32 v173, v173
	v_exp_f32_e32 v174, v174
	v_exp_f32_e32 v175, v175
	v_add_f32_e32 v254, v254, v172
	v_add_f32_e32 v254, v254, v173
	v_add_f32_e32 v254, v254, v174
	v_add_f32_e32 v254, v254, v175
	v_cvt_pk_bf16_f32 v164, v168, v169
	v_cvt_pk_bf16_f32 v165, v170, v171
	v_sub_f32_e32 v176, v176, v229
	v_sub_f32_e32 v177, v177, v229
	v_sub_f32_e32 v178, v178, v229
	s_waitcnt lgkmcnt(2)
	v_mfma_f32_32x32x16_bf16 v[128:143], v[196:199], v[192:195], v[128:143]
	v_sub_f32_e32 v179, v179, v229
	v_exp_f32_e32 v176, v176
	v_exp_f32_e32 v177, v177
	v_exp_f32_e32 v178, v178
	v_exp_f32_e32 v179, v179
	v_add_f32_e32 v255, v176, v177
	v_add_f32_e32 v255, v255, v178
	v_add_f32_e32 v255, v255, v179
	v_cvt_pk_bf16_f32 v166, v172, v173
	v_cvt_pk_bf16_f32 v167, v174, v175
	v_sub_f32_e32 v180, v180, v229
	v_sub_f32_e32 v181, v181, v229
	v_sub_f32_e32 v182, v182, v229
	s_waitcnt lgkmcnt(1)
	v_mfma_f32_32x32x16_bf16 v[144:159], v[200:203], v[192:195], v[144:159]
	v_add3_u32 v230, v237, v247, s48
	ds_read_b128 v[196:199], v230
	ds_read_b128 v[200:203], v230 offset:8192
	v_sub_f32_e32 v183, v183, v229
	v_exp_f32_e32 v180, v180
	v_exp_f32_e32 v181, v181
	v_exp_f32_e32 v182, v182
	v_exp_f32_e32 v183, v183
	v_add_f32_e32 v255, v255, v180
	v_add_f32_e32 v255, v255, v181
	v_add_f32_e32 v255, v255, v182
	v_add_f32_e32 v255, v255, v183
	v_cvt_pk_bf16_f32 v168, v176, v177
	v_cvt_pk_bf16_f32 v169, v178, v179
	v_sub_f32_e32 v184, v184, v229
	v_sub_f32_e32 v185, v185, v229
	s_waitcnt lgkmcnt(1)
	v_mfma_f32_32x32x16_bf16 v[128:143], v[196:199], v[204:207], v[128:143]
	v_sub_f32_e32 v186, v186, v229
	v_sub_f32_e32 v187, v187, v229
	v_exp_f32_e32 v184, v184
	v_exp_f32_e32 v185, v185
	v_exp_f32_e32 v186, v186
	v_exp_f32_e32 v187, v187
	v_add_f32_e32 v255, v255, v184
	v_add_f32_e32 v255, v255, v185
	v_add_f32_e32 v255, v255, v186
	v_add_f32_e32 v255, v255, v187
	v_cvt_pk_bf16_f32 v170, v180, v181
	v_cvt_pk_bf16_f32 v171, v182, v183
	v_sub_f32_e32 v188, v188, v229
	v_sub_f32_e32 v189, v189, v229
	s_waitcnt lgkmcnt(0)
	v_mfma_f32_32x32x16_bf16 v[144:159], v[200:203], v[204:207], v[144:159]
	v_sub_f32_e32 v190, v190, v229
	v_sub_f32_e32 v191, v191, v229
	v_exp_f32_e32 v188, v188
	v_exp_f32_e32 v189, v189
	v_exp_f32_e32 v190, v190
	v_exp_f32_e32 v191, v191
	v_add_f32_e32 v255, v255, v188
	v_add_f32_e32 v255, v255, v189
	v_add_f32_e32 v255, v255, v190
	v_add_f32_e32 v255, v255, v191
	v_cvt_pk_bf16_f32 v172, v184, v185
	v_cvt_pk_bf16_f32 v173, v186, v187
	v_cvt_pk_bf16_f32 v174, v188, v189
	v_cvt_pk_bf16_f32 v175, v190, v191
	v_add_f32_e32 v254, v254, v255
	v_add_f32_e32 v251, v251, v254
	s_branch .Lattn_mid

.Lattn_nobias1_c:
	v_max3_f32 v228, v128, v129, v130
	v_max3_f32 v229, v131, v132, v133
	s_waitcnt lgkmcnt(4)
	v_mfma_f32_32x32x16_bf16 v[64:79], v[160:163], v[176:179], v[64:79]
	ds_read_b64_tr_b16 v[188:189], v215 offset:32768
	ds_read_b64_tr_b16 v[190:191], v215 offset:34816
	v_max3_f32 v228, v228, v134, v135
	v_max3_f32 v229, v229, v136, v137
	s_add_i32 s17, s41, 1
	s_cmp_lt_u32 s17, s42
	s_cbranch_scc0 .Lattn_nok0_c
	s_add_u32 s18, s14, 0x68000
	s_addc_u32 s19, s15, 0
	v_lshl_add_u64 v[254:255], v[210:211], 0, s[18:19]
	s_add_i32 s17, s44, s48
	s_mov_b32 m0, s17
	s_nop 0
	global_load_lds_dwordx4 v[254:255], off
.Lattn_nok0_c:
	v_max3_f32 v228, v228, v138, v139
	v_max3_f32 v229, v229, v140, v141
	v_max3_f32 v228, v228, v142, v143
	v_max3_f32 v229, v229, v144, v145
	s_waitcnt lgkmcnt(4)
	v_mfma_f32_32x32x16_bf16 v[32:47], v[160:163], v[180:183], v[32:47]
	ds_read_b64_tr_b16 v[176:177], v212 offset:36864
	ds_read_b64_tr_b16 v[178:179], v212 offset:38912
	s_cmp_lt_u32 s41, s42
	s_cbranch_scc0 .Lattn_nov0_c
	v_lshl_add_u64 v[254:255], v[218:219], 0, s[14:15]
	s_add_i32 s17, s44, s51
	s_add_i32 m0, s17, 0x8000
	s_nop 0
	global_load_lds_dwordx4 v[254:255], off
.Lattn_nov0_c:
	v_max3_f32 v228, v228, v146, v147
	v_max3_f32 v229, v229, v148, v149
	v_max3_f32 v228, v228, v150, v151
	v_max3_f32 v229, v229, v152, v153
	s_add_i32 s17, s41, 1
	s_cmp_lt_u32 s17, s42
	s_cbranch_scc0 .Lattn_nok1_c
	s_add_u32 s18, s14, 0x68000
	s_addc_u32 s19, s15, 0
	v_lshl_add_u64 v[254:255], v[216:217], 0, s[18:19]
	s_add_i32 s17, s44, s48
	s_add_i32 m0, s17, 0x400
	s_nop 0
	global_load_lds_dwordx4 v[254:255], off
.Lattn_nok1_c:
	v_max3_f32 v228, v228, v154, v155
	s_waitcnt lgkmcnt(4)
	v_mfma_f32_32x32x16_bf16 v[16:31], v[160:163], v[184:187], v[16:31]
	ds_read_b64_tr_b16 v[180:181], v213 offset:36864
	ds_read_b64_tr_b16 v[182:183], v213 offset:38912
	v_max3_f32 v229, v229, v156, v157
	v_max3_f32 v228, v228, v158, v159
	v_max_f32_e32 v228, v228, v229
	s_cmp_lt_u32 s41, s42
	s_cbranch_scc0 .Lattn_nov1_c
	v_lshl_add_u64 v[254:255], v[220:221], 0, s[14:15]
	s_add_i32 s17, s44, s51
	s_add_i32 m0, s17, 0x8400
	s_nop 0
	global_load_lds_dwordx4 v[254:255], off
.Lattn_nov1_c:
	v_mov_b32_e32 v229, v228
	s_nop 1
	v_permlane32_swap_b32_e32 v228, v229
	v_max_f32_e32 v228, v228, v229
	v_add_f32_e32 v228, s49, v228
	v_sub_f32_e32 v229, v228, v227
	v_cmp_lt_f32_e32 vcc, 0x41000000, v229
	s_cbranch_vccz .Lattn_noresc1_c
	s_nop 0
	v_cndmask_b32_e32 v229, v227, v228, vcc
	v_sub_f32_e32 v228, v227, v229
	v_exp_f32_e32 v228, v228
	v_mov_b32_e32 v227, v229
	ds_write_b32 v239, v228
	ds_read_b128 v[192:195], v249
	ds_read_b128 v[196:199], v249 offset:32
	ds_read_b128 v[200:203], v249 offset:64
	ds_read_b128 v[204:207], v249 offset:96
	v_mul_f32_e32 v208, v208, v228
	s_waitcnt lgkmcnt(3)
	v_pk_mul_f32 v[112:113], v[112:113], v[192:193]
	v_pk_mul_f32 v[114:115], v[114:115], v[194:195]
	v_pk_mul_f32 v[96:97], v[96:97], v[192:193]
	v_pk_mul_f32 v[98:99], v[98:99], v[194:195]
	v_pk_mul_f32 v[80:81], v[80:81], v[192:193]
	v_pk_mul_f32 v[82:83], v[82:83], v[194:195]
	v_pk_mul_f32 v[48:49], v[48:49], v[192:193]
	v_pk_mul_f32 v[50:51], v[50:51], v[194:195]
	s_waitcnt lgkmcnt(2)
	v_pk_mul_f32 v[116:117], v[116:117], v[196:197]
	v_pk_mul_f32 v[118:119], v[118:119], v[198:199]
	v_pk_mul_f32 v[100:101], v[100:101], v[196:197]
	v_pk_mul_f32 v[102:103], v[102:103], v[198:199]
	v_pk_mul_f32 v[84:85], v[84:85], v[196:197]
	v_pk_mul_f32 v[86:87], v[86:87], v[198:199]
	v_pk_mul_f32 v[52:53], v[52:53], v[196:197]
	v_pk_mul_f32 v[54:55], v[54:55], v[198:199]
	s_waitcnt lgkmcnt(1)
	v_pk_mul_f32 v[120:121], v[120:121], v[200:201]
	v_pk_mul_f32 v[122:123], v[122:123], v[202:203]
	v_pk_mul_f32 v[104:105], v[104:105], v[200:201]
	v_pk_mul_f32 v[106:107], v[106:107], v[202:203]
	v_pk_mul_f32 v[88:89], v[88:89], v[200:201]
	v_pk_mul_f32 v[90:91], v[90:91], v[202:203]
	v_pk_mul_f32 v[56:57], v[56:57], v[200:201]
	v_pk_mul_f32 v[58:59], v[58:59], v[202:203]
	s_waitcnt lgkmcnt(0)
	v_pk_mul_f32 v[124:125], v[124:125], v[204:205]
	v_pk_mul_f32 v[126:127], v[126:127], v[206:207]
	v_pk_mul_f32 v[108:109], v[108:109], v[204:205]
	v_pk_mul_f32 v[110:111], v[110:111], v[206:207]
	v_pk_mul_f32 v[92:93], v[92:93], v[204:205]
	v_pk_mul_f32 v[94:95], v[94:95], v[206:207]
	v_pk_mul_f32 v[60:61], v[60:61], v[204:205]
	v_pk_mul_f32 v[62:63], v[62:63], v[206:207]
.Lattn_noresc1_c:
	v_subrev_f32_e32 v229, s49, v227
	ds_read_b64_tr_b16 v[184:185], v214 offset:36864
	ds_read_b64_tr_b16 v[186:187], v214 offset:38912
	ds_read_b64_tr_b16 v[192:193], v215 offset:36864
	ds_read_b64_tr_b16 v[194:195], v215 offset:38912
	ds_read_b64_tr_b16 v[196:197], v212 offset:40960
	ds_read_b64_tr_b16 v[198:199], v212 offset:43008
	ds_read_b64_tr_b16 v[200:201], v213 offset:40960
	ds_read_b64_tr_b16 v[202:203], v213 offset:43008
	v_sub_f32_e32 v128, v128, v229
	v_sub_f32_e32 v129, v129, v229
	v_sub_f32_e32 v130, v130, v229
	s_waitcnt lgkmcnt(12)
	v_mfma_f32_32x32x16_bf16 v[0:15], v[160:163], v[188:191], v[0:15]
	ds_read_b64_tr_b16 v[204:205], v214 offset:40960
	ds_read_b64_tr_b16 v[206:207], v214 offset:43008
	v_sub_f32_e32 v131, v131, v229
	v_exp_f32_e32 v128, v128
	v_exp_f32_e32 v129, v129
	v_exp_f32_e32 v130, v130
	s_waitcnt lgkmcnt(12)
	v_mfma_f32_32x32x16_bf16 v[64:79], v[164:167], v[176:179], v[64:79]
	ds_read_b64_tr_b16 v[188:189], v215 offset:40960
	ds_read_b64_tr_b16 v[190:191], v215 offset:43008
	v_exp_f32_e32 v131, v131
	v_add_f32_e32 v254, v128, v129
	v_add_f32_e32 v254, v254, v130
	v_add_f32_e32 v254, v254, v131
	v_sub_f32_e32 v132, v132, v229
	s_waitcnt lgkmcnt(12)
	v_mfma_f32_32x32x16_bf16 v[32:47], v[164:167], v[180:183], v[32:47]
	ds_read_b64_tr_b16 v[176:177], v212 offset:45056
	ds_read_b64_tr_b16 v[178:179], v212 offset:47104
	v_sub_f32_e32 v133, v133, v229
	v_sub_f32_e32 v134, v134, v229
	v_sub_f32_e32 v135, v135, v229
	v_exp_f32_e32 v132, v132
	s_waitcnt lgkmcnt(12)
	v_mfma_f32_32x32x16_bf16 v[16:31], v[164:167], v[184:187], v[16:31]
	ds_read_b64_tr_b16 v[180:181], v213 offset:45056
	ds_read_b64_tr_b16 v[182:183], v213 offset:47104
	v_exp_f32_e32 v133, v133
	v_exp_f32_e32 v134, v134
	v_exp_f32_e32 v135, v135
	v_add_f32_e32 v254, v254, v132
	v_add_f32_e32 v254, v254, v133
	s_waitcnt lgkmcnt(12)
	v_mfma_f32_32x32x16_bf16 v[0:15], v[164:167], v[192:195], v[0:15]
	ds_read_b64_tr_b16 v[184:185], v214 offset:45056
	ds_read_b64_tr_b16 v[186:187], v214 offset:47104
	v_add_f32_e32 v254, v254, v134
	v_add_f32_e32 v254, v254, v135
	v_cvt_pk_bf16_f32 v128, v128, v129
	v_cvt_pk_bf16_f32 v129, v130, v131
	v_sub_f32_e32 v136, v136, v229
	s_waitcnt lgkmcnt(12)
	v_mfma_f32_32x32x16_bf16 v[64:79], v[168:171], v[196:199], v[64:79]
	ds_read_b64_tr_b16 v[192:193], v215 offset:45056
	ds_read_b64_tr_b16 v[194:195], v215 offset:47104
	v_sub_f32_e32 v137, v137, v229
	v_sub_f32_e32 v138, v138, v229
	v_sub_f32_e32 v139, v139, v229
	v_exp_f32_e32 v136, v136
	s_waitcnt lgkmcnt(12)
	v_mfma_f32_32x32x16_bf16 v[32:47], v[168:171], v[200:203], v[32:47]
	ds_read_b128 v[196:199], v240
	v_exp_f32_e32 v137, v137
	v_exp_f32_e32 v138, v138
	v_exp_f32_e32 v139, v139
	v_add_f32_e32 v254, v254, v136
	v_add_f32_e32 v254, v254, v137
	s_waitcnt lgkmcnt(11)
	v_mfma_f32_32x32x16_bf16 v[16:31], v[168:171], v[204:207], v[16:31]
	v_add3_u32 v230, v237, v240, s51
	ds_read_b128 v[200:203], v230
	ds_read_b128 v[204:207], v230 offset:8192
	v_add_f32_e32 v254, v254, v138
	v_add_f32_e32 v254, v254, v139
	v_cvt_pk_bf16_f32 v130, v132, v133
	v_cvt_pk_bf16_f32 v131, v134, v135
	v_sub_f32_e32 v140, v140, v229
	s_waitcnt lgkmcnt(11)
	v_mfma_f32_32x32x16_bf16 v[0:15], v[168:171], v[188:191], v[0:15]
	v_sub_f32_e32 v141, v141, v229
	v_sub_f32_e32 v142, v142, v229
	v_sub_f32_e32 v143, v143, v229
	v_exp_f32_e32 v140, v140
	s_waitcnt lgkmcnt(9)
	v_mfma_f32_32x32x16_bf16 v[64:79], v[172:175], v[176:179], v[64:79]
	v_exp_f32_e32 v141, v141
	v_exp_f32_e32 v142, v142
	v_exp_f32_e32 v143, v143
	v_add_f32_e32 v254, v254, v140
	v_add_f32_e32 v254, v254, v141
	s_waitcnt lgkmcnt(7)
	v_mfma_f32_32x32x16_bf16 v[32:47], v[172:175], v[180:183], v[32:47]
	v_add_f32_e32 v254, v254, v142
	v_add_f32_e32 v254, v254, v143
	v_cvt_pk_bf16_f32 v132, v136, v137
	v_cvt_pk_bf16_f32 v133, v138, v139
	v_sub_f32_e32 v144, v144, v229
	s_waitcnt lgkmcnt(5)
	v_mfma_f32_32x32x16_bf16 v[16:31], v[172:175], v[184:187], v[16:31]
	v_sub_f32_e32 v145, v145, v229
	v_sub_f32_e32 v146, v146, v229
	v_sub_f32_e32 v147, v147, v229
	v_exp_f32_e32 v144, v144
	s_waitcnt lgkmcnt(3)
	v_mfma_f32_32x32x16_bf16 v[0:15], v[172:175], v[192:195], v[0:15]
	ds_read_b128 v[192:195], v241
	v_exp_f32_e32 v145, v145
	v_exp_f32_e32 v146, v146
	v_exp_f32_e32 v147, v147
	v_add_f32_e32 v255, v144, v145
	v_add_f32_e32 v255, v255, v146
	s_waitcnt lgkmcnt(2)
	v_mfma_f32_32x32x16_bf16 v[160:175], v[200:203], v[196:199], 0
	v_add_f32_e32 v255, v255, v147
	v_cvt_pk_bf16_f32 v134, v140, v141
	v_cvt_pk_bf16_f32 v135, v142, v143
	v_sub_f32_e32 v148, v148, v229
	v_sub_f32_e32 v149, v149, v229
	s_waitcnt lgkmcnt(1)
	v_mfma_f32_32x32x16_bf16 v[176:191], v[204:207], v[196:199], 0
	v_add3_u32 v230, v237, v241, s51
	ds_read_b128 v[200:203], v230
	ds_read_b128 v[204:207], v230 offset:8192
	ds_read_b128 v[196:199], v242
	v_sub_f32_e32 v150, v150, v229
	v_sub_f32_e32 v151, v151, v229
	v_exp_f32_e32 v148, v148
	v_exp_f32_e32 v149, v149
	s_waitcnt lgkmcnt(2)
	v_mfma_f32_32x32x16_bf16 v[160:175], v[200:203], v[192:195], v[160:175]
	v_exp_f32_e32 v150, v150
	v_exp_f32_e32 v151, v151
	v_add_f32_e32 v255, v255, v148
	v_add_f32_e32 v255, v255, v149
	v_add_f32_e32 v255, v255, v150
	s_waitcnt lgkmcnt(1)
	v_mfma_f32_32x32x16_bf16 v[176:191], v[204:207], v[192:195], v[176:191]
	v_add3_u32 v230, v237, v242, s51
	ds_read_b128 v[200:203], v230
	ds_read_b128 v[204:207], v230 offset:8192
	ds_read_b128 v[192:195], v243
	v_add_f32_e32 v255, v255, v151
	v_cvt_pk_bf16_f32 v136, v144, v145
	v_cvt_pk_bf16_f32 v137, v146, v147
	v_sub_f32_e32 v152, v152, v229
	v_sub_f32_e32 v153, v153, v229
	s_waitcnt lgkmcnt(2)
	v_mfma_f32_32x32x16_bf16 v[160:175], v[200:203], v[196:199], v[160:175]
	v_sub_f32_e32 v154, v154, v229
	v_sub_f32_e32 v155, v155, v229
	v_exp_f32_e32 v152, v152
	v_exp_f32_e32 v153, v153
	s_waitcnt lgkmcnt(1)
	v_mfma_f32_32x32x16_bf16 v[176:191], v[204:207], v[196:199], v[176:191]
	v_add3_u32 v230, v237, v243, s51
	ds_read_b128 v[200:203], v230
	ds_read_b128 v[204:207], v230 offset:8192
	v_exp_f32_e32 v154, v154
	v_exp_f32_e32 v155, v155
	v_add_f32_e32 v255, v255, v152
	v_add_f32_e32 v255, v255, v153
	v_add_f32_e32 v255, v255, v154
	s_waitcnt lgkmcnt(1)
	v_mfma_f32_32x32x16_bf16 v[160:175], v[200:203], v[192:195], v[160:175]
	v_add_f32_e32 v255, v255, v155
	v_cvt_pk_bf16_f32 v138, v148, v149
	v_cvt_pk_bf16_f32 v139, v150, v151
	v_sub_f32_e32 v156, v156, v229
	v_sub_f32_e32 v157, v157, v229
	s_waitcnt lgkmcnt(0)
	v_mfma_f32_32x32x16_bf16 v[176:191], v[204:207], v[192:195], v[176:191]
	v_sub_f32_e32 v158, v158, v229
	v_sub_f32_e32 v159, v159, v229
	v_exp_f32_e32 v156, v156
	v_exp_f32_e32 v157, v157
	v_exp_f32_e32 v158, v158
	v_exp_f32_e32 v159, v159
	v_add_f32_e32 v255, v255, v156
	v_add_f32_e32 v255, v255, v157
	v_add_f32_e32 v255, v255, v158
	v_add_f32_e32 v255, v255, v159
	v_cvt_pk_bf16_f32 v140, v152, v153
	v_cvt_pk_bf16_f32 v141, v154, v155
	v_cvt_pk_bf16_f32 v142, v156, v157
	v_cvt_pk_bf16_f32 v143, v158, v159
	v_add_f32_e32 v254, v254, v255
	v_add_f32_e32 v208, v208, v254
	s_branch .Lattn_tail

.Lattn_noresc1_d:
	v_subrev_f32_e32 v229, s49, v227
	ds_read_b64_tr_b16 v[184:185], v214 offset:36864
	ds_read_b64_tr_b16 v[186:187], v214 offset:38912
	ds_read_b64_tr_b16 v[192:193], v215 offset:36864
	ds_read_b64_tr_b16 v[194:195], v215 offset:38912
	ds_read_b64_tr_b16 v[196:197], v212 offset:40960
	ds_read_b64_tr_b16 v[198:199], v212 offset:43008
	ds_read_b64_tr_b16 v[200:201], v213 offset:40960
	ds_read_b64_tr_b16 v[202:203], v213 offset:43008
	v_sub_f32_e32 v128, v128, v229
	v_sub_f32_e32 v129, v129, v229
	v_sub_f32_e32 v130, v130, v229
	s_waitcnt lgkmcnt(12)
	v_mfma_f32_32x32x16_bf16 v[0:15], v[160:163], v[188:191], v[0:15]
	ds_read_b64_tr_b16 v[204:205], v214 offset:40960
	ds_read_b64_tr_b16 v[206:207], v214 offset:43008
	v_sub_f32_e32 v131, v131, v229
	v_exp_f32_e32 v128, v128
	v_exp_f32_e32 v129, v129
	v_exp_f32_e32 v130, v130
	v_exp_f32_e32 v131, v131
	v_add_f32_e32 v254, v128, v129
	v_add_f32_e32 v254, v254, v130
	s_waitcnt lgkmcnt(12)
	v_mfma_f32_32x32x16_bf16 v[64:79], v[164:167], v[176:179], v[64:79]
	ds_read_b64_tr_b16 v[188:189], v215 offset:40960
	ds_read_b64_tr_b16 v[190:191], v215 offset:43008
	v_add_f32_e32 v254, v254, v131
	v_sub_f32_e32 v132, v132, v229
	v_sub_f32_e32 v133, v133, v229
	v_sub_f32_e32 v134, v134, v229
	v_sub_f32_e32 v135, v135, v229
	v_exp_f32_e32 v132, v132
	v_exp_f32_e32 v133, v133
	v_exp_f32_e32 v134, v134
	s_waitcnt lgkmcnt(12)
	v_mfma_f32_32x32x16_bf16 v[32:47], v[164:167], v[180:183], v[32:47]
	ds_read_b64_tr_b16 v[176:177], v212 offset:45056
	ds_read_b64_tr_b16 v[178:179], v212 offset:47104
	v_exp_f32_e32 v135, v135
	v_add_f32_e32 v254, v254, v132
	v_add_f32_e32 v254, v254, v133
	v_add_f32_e32 v254, v254, v134
	v_add_f32_e32 v254, v254, v135
	v_cvt_pk_bf16_f32 v128, v128, v129
	v_cvt_pk_bf16_f32 v129, v130, v131
	v_sub_f32_e32 v136, v136, v229
	s_waitcnt lgkmcnt(12)
	v_mfma_f32_32x32x16_bf16 v[16:31], v[164:167], v[184:187], v[16:31]
	ds_read_b64_tr_b16 v[180:181], v213 offset:45056
	ds_read_b64_tr_b16 v[182:183], v213 offset:47104
	v_sub_f32_e32 v137, v137, v229
	v_sub_f32_e32 v138, v138, v229
	v_sub_f32_e32 v139, v139, v229
	v_exp_f32_e32 v136, v136
	v_exp_f32_e32 v137, v137
	v_exp_f32_e32 v138, v138
	v_exp_f32_e32 v139, v139
	v_add_f32_e32 v254, v254, v136
	s_waitcnt lgkmcnt(12)
	v_mfma_f32_32x32x16_bf16 v[0:15], v[164:167], v[192:195], v[0:15]
	ds_read_b64_tr_b16 v[184:185], v214 offset:45056
	ds_read_b64_tr_b16 v[186:187], v214 offset:47104
	v_add_f32_e32 v254, v254, v137
	v_add_f32_e32 v254, v254, v138
	v_add_f32_e32 v254, v254, v139
	v_cvt_pk_bf16_f32 v130, v132, v133
	v_cvt_pk_bf16_f32 v131, v134, v135
	v_sub_f32_e32 v140, v140, v229
	v_sub_f32_e32 v141, v141, v229
	s_waitcnt lgkmcnt(12)
	v_mfma_f32_32x32x16_bf16 v[64:79], v[168:171], v[196:199], v[64:79]
	ds_read_b64_tr_b16 v[192:193], v215 offset:45056
	ds_read_b64_tr_b16 v[194:195], v215 offset:47104
	v_sub_f32_e32 v142, v142, v229
	v_sub_f32_e32 v143, v143, v229
	v_exp_f32_e32 v140, v140
	v_exp_f32_e32 v141, v141
	v_exp_f32_e32 v142, v142
	v_exp_f32_e32 v143, v143
	v_add_f32_e32 v254, v254, v140
	v_add_f32_e32 v254, v254, v141
	s_waitcnt lgkmcnt(12)
	v_mfma_f32_32x32x16_bf16 v[32:47], v[168:171], v[200:203], v[32:47]
	v_add_f32_e32 v254, v254, v142
	v_add_f32_e32 v254, v254, v143
	v_cvt_pk_bf16_f32 v132, v136, v137
	v_cvt_pk_bf16_f32 v133, v138, v139
	v_sub_f32_e32 v144, v144, v229
	v_sub_f32_e32 v145, v145, v229
	v_sub_f32_e32 v146, v146, v229
	v_sub_f32_e32 v147, v147, v229
	s_waitcnt lgkmcnt(10)
	v_mfma_f32_32x32x16_bf16 v[16:31], v[168:171], v[204:207], v[16:31]
	v_exp_f32_e32 v144, v144
	v_exp_f32_e32 v145, v145
	v_exp_f32_e32 v146, v146
	v_exp_f32_e32 v147, v147
	v_add_f32_e32 v255, v144, v145
	v_add_f32_e32 v255, v255, v146
	v_add_f32_e32 v255, v255, v147
	v_cvt_pk_bf16_f32 v134, v140, v141
	s_waitcnt lgkmcnt(8)
	v_mfma_f32_32x32x16_bf16 v[0:15], v[168:171], v[188:191], v[0:15]
	v_cvt_pk_bf16_f32 v135, v142, v143
	v_sub_f32_e32 v148, v148, v229
	v_sub_f32_e32 v149, v149, v229
	v_sub_f32_e32 v150, v150, v229
	v_sub_f32_e32 v151, v151, v229
	v_exp_f32_e32 v148, v148
	v_exp_f32_e32 v149, v149
	s_waitcnt lgkmcnt(6)
	v_mfma_f32_32x32x16_bf16 v[64:79], v[172:175], v[176:179], v[64:79]
	v_exp_f32_e32 v150, v150
	v_exp_f32_e32 v151, v151
	v_add_f32_e32 v255, v255, v148
	v_add_f32_e32 v255, v255, v149
	v_add_f32_e32 v255, v255, v150
	v_add_f32_e32 v255, v255, v151
	v_cvt_pk_bf16_f32 v136, v144, v145
	v_cvt_pk_bf16_f32 v137, v146, v147
	s_waitcnt lgkmcnt(4)
	v_mfma_f32_32x32x16_bf16 v[32:47], v[172:175], v[180:183], v[32:47]
	v_sub_f32_e32 v152, v152, v229
	v_sub_f32_e32 v153, v153, v229
	v_sub_f32_e32 v154, v154, v229
	v_sub_f32_e32 v155, v155, v229
	v_exp_f32_e32 v152, v152
	v_exp_f32_e32 v153, v153
	v_exp_f32_e32 v154, v154
	v_exp_f32_e32 v155, v155
	s_waitcnt lgkmcnt(2)
	v_mfma_f32_32x32x16_bf16 v[16:31], v[172:175], v[184:187], v[16:31]
	v_add_f32_e32 v255, v255, v152
	v_add_f32_e32 v255, v255, v153
	v_add_f32_e32 v255, v255, v154
	v_add_f32_e32 v255, v255, v155
	v_cvt_pk_bf16_f32 v138, v148, v149
	v_cvt_pk_bf16_f32 v139, v150, v151
	v_sub_f32_e32 v156, v156, v229
	v_sub_f32_e32 v157, v157, v229
	s_waitcnt lgkmcnt(0)
	v_mfma_f32_32x32x16_bf16 v[0:15], v[172:175], v[192:195], v[0:15]
	v_sub_f32_e32 v158, v158, v229
	v_sub_f32_e32 v159, v159, v229
	v_exp_f32_e32 v156, v156
	v_exp_f32_e32 v157, v157
	v_exp_f32_e32 v158, v158
	v_exp_f32_e32 v159, v159
	v_add_f32_e32 v255, v255, v156
	v_add_f32_e32 v255, v255, v157
	v_add_f32_e32 v255, v255, v158
	v_add_f32_e32 v255, v255, v159
	v_cvt_pk_bf16_f32 v140, v152, v153
	v_cvt_pk_bf16_f32 v141, v154, v155
	v_cvt_pk_bf16_f32 v142, v156, v157
	v_cvt_pk_bf16_f32 v143, v158, v159
	v_add_f32_e32 v254, v254, v255
	v_add_f32_e32 v208, v208, v254
	s_branch .Lattn_tail
